# nt hint also on the prologue (layer 0) weight-conversion loads and stores
# speedup vs baseline: 1.0221x; 1.0037x over previous
; __device__ __forceinline__ unsigned pk4_fp8(float x0, float x1, float x2, float x3) { int w = 0; w = __builtin_amdgcn_cvt_pk_fp8_f32(x0, x1, w, false); w = __builtin_amdgcn_cvt_pk_fp8_f32(x2, x3, w, true); return (unsigned)w; }
; __device__ __forceinline__ void transpose_item_fp8w(const float* W, int K, int N, unsigned char* WT, float q, LAS unsigned char* scr, int item, int lane) {
;     const int nblk = N / 128, kb = item / nblk, nb = item % nblk, k0 = 64 * kb, n0 = 128 * nb;
;     const int l5 = lane & 31, h = lane >> 5;
;     const float* src = W + (size_t)(k0 + 16 * h) * N + n0 + 4 * l5;
; #pragma unroll
;     for (int b = 0; b < 2; ++b) {
;         f32x4 x[16];
; #pragma unroll
;         for (int s_ = 0; s_ < 16; ++s_) x[s_] = *(const f32x4*)(src + (size_t)(32 * b + s_) * N);
; #pragma unroll
;         for (int i = 0; i < 4; ++i) {
;             u32x4 o;
;             o.x = pk4_fp8(x[0][i] * q, x[1][i] * q, x[2][i] * q, x[3][i] * q); o.y = pk4_fp8(x[4][i] * q, x[5][i] * q, x[6][i] * q, x[7][i] * q);
.LBB0_38:
	s_cmpk_gt_i32 s66, 0x3df
	s_mov_b64 s[6:7], -1
	s_cbranch_scc0 .LBB0_70
	s_cmpk_gt_u32 s66, 0x46f
	s_cbranch_scc0 .LBB0_57
	s_cmpk_gt_u32 s66, 0x4ef
	s_cbranch_scc0 .LBB0_52
	s_cmpk_gt_u32 s66, 0x6ef
	s_cbranch_scc0 .LBB0_47
	s_cmpk_gt_u32 s66, 0x26ef
	v_lshlrev_b32_e32 v142, 2, v140
	v_add_u32_e32 v195, v179, v180
	s_cbranch_scc0 .LBB0_44
	s_add_i32 s67, s66, 0xffffd910
	s_lshr_b32 s4, s67, 7
	s_lshl_b64 s[8:9], s[4:5], 20
	s_lshl_b64 s[6:7], s[4:5], 22
	s_add_u32 s68, s16, s6
	s_addc_u32 s69, s17, s7
	v_readlane_b32 s4, v246, 17
	s_add_u32 s7, s4, s8
	v_readlane_b32 s4, v246, 18
	s_addc_u32 s8, s4, s9
	s_lshl_b32 s4, s67, 6
	s_and_b32 s9, s4, 0x3c0
	v_add_u32_e32 v0, s9, v177
	s_lshl_b32 s4, s67, 3
	v_ashrrev_i32_e32 v1, 31, v0
	s_and_b32 s6, s4, 0x380
	v_lshlrev_b64 v[0:1], 12, v[0:1]
	v_lshl_add_u64 v[0:1], s[68:69], 0, v[0:1]
	s_lshl_b32 s4, s6, 2
	v_lshl_add_u64 v[0:1], v[0:1], 0, s[4:5]
	v_lshl_add_u64 v[80:81], v[0:1], 0, v[142:143]
	v_add_co_u32_e32 v8, vcc, s10, v80
	global_load_dwordx4 v[0:3], v[80:81], off nt
	s_nop 0
	v_addc_co_u32_e32 v9, vcc, 0, v81, vcc
	v_add_co_u32_e32 v12, vcc, s11, v80
	global_load_dwordx4 v[4:7], v[8:9], off offset:-4096 nt
	s_nop 0
	global_load_dwordx4 v[8:11], v[8:9], off nt
	v_addc_co_u32_e32 v13, vcc, 0, v81, vcc
	v_add_co_u32_e32 v16, vcc, s15, v80
	global_load_dwordx4 v[20:23], v[12:13], off offset:-4096 nt
	s_nop 0
	global_load_dwordx4 v[12:15], v[12:13], off nt
	v_addc_co_u32_e32 v17, vcc, 0, v81, vcc
	v_add_co_u32_e32 v28, vcc, s20, v80
	global_load_dwordx4 v[24:27], v[16:17], off offset:-4096 nt
	s_nop 0
	global_load_dwordx4 v[16:19], v[16:17], off nt
	v_addc_co_u32_e32 v29, vcc, 0, v81, vcc
	v_add_co_u32_e32 v40, vcc, s21, v80
	global_load_dwordx4 v[32:35], v[28:29], off offset:-4096 nt
	s_nop 0
	global_load_dwordx4 v[28:31], v[28:29], off nt
	v_addc_co_u32_e32 v41, vcc, 0, v81, vcc
	v_add_co_u32_e32 v44, vcc, s22, v80
	global_load_dwordx4 v[36:39], v[40:41], off offset:-4096 nt
	s_nop 0
	global_load_dwordx4 v[40:43], v[40:41], off nt
	v_addc_co_u32_e32 v45, vcc, 0, v81, vcc
	v_add_co_u32_e32 v48, vcc, s23, v80
	global_load_dwordx4 v[52:55], v[44:45], off offset:-4096 nt
	s_nop 0
	global_load_dwordx4 v[44:47], v[44:45], off nt
	v_addc_co_u32_e32 v49, vcc, 0, v81, vcc
	global_load_dwordx4 v[56:59], v[48:49], off offset:-4096 nt
	s_nop 0
	global_load_dwordx4 v[48:51], v[48:49], off nt
	v_add_co_u32_e32 v60, vcc, s24, v80
	v_mov_b32_e32 v64, v143
	s_nop 0
	v_addc_co_u32_e32 v61, vcc, 0, v81, vcc
	global_load_dwordx4 v[60:63], v[60:61], off nt
	v_mov_b32_e32 v68, v143
	v_mov_b32_e32 v69, v143
	v_mov_b32_e32 v70, v143
	v_mov_b32_e32 v71, v143
	v_mov_b32_e32 v136, v143
	v_mov_b32_e32 v137, v143
	v_mov_b32_e32 v138, v143
	v_mov_b32_e32 v139, v143
	v_mov_b32_e32 v65, v143
	v_mov_b32_e32 v66, v143
	v_mov_b32_e32 v67, v143
	s_add_u32 s68, s7, s9
	s_addc_u32 s69, s8, 0
	s_waitcnt vmcnt(15)
	v_mul_f32_e32 v0, 0x43800000, v0
	v_mul_f32_e32 v1, 0x43800000, v1
	s_waitcnt vmcnt(14)
	v_mul_f32_e32 v4, 0x43800000, v4
	v_mul_f32_e32 v5, 0x43800000, v5
	v_cvt_pk_fp8_f32 v64, v0, v4
	v_cvt_pk_fp8_f32 v68, v1, v5
	s_waitcnt vmcnt(13)
	v_mul_f32_e32 v8, 0x43800000, v8
	s_waitcnt vmcnt(12)
	v_mul_f32_e32 v20, 0x43800000, v20
	s_waitcnt vmcnt(11)
	v_mul_f32_e32 v0, 0x43800000, v13
	v_mul_f32_e32 v12, 0x43800000, v12
	v_mul_f32_e32 v9, 0x43800000, v9
	v_mul_f32_e32 v21, 0x43800000, v21
	s_waitcnt vmcnt(10)
	v_mul_f32_e32 v1, 0x43800000, v25
	v_cvt_pk_fp8_f32 v69, v0, v1
	s_waitcnt vmcnt(9)
	v_mul_f32_e32 v0, 0x43800000, v17
	v_mul_f32_e32 v24, 0x43800000, v24
	v_cvt_pk_fp8_f32 v65, v12, v24
	s_waitcnt vmcnt(8)
	v_mul_f32_e32 v1, 0x43800000, v33
	v_cvt_pk_fp8_f32 v69, v0, v1 op_sel:[0,0,1]
	s_waitcnt vmcnt(7)
	v_mul_f32_e32 v0, 0x43800000, v29
	v_mul_f32_e32 v28, 0x43800000, v28
	v_mul_f32_e32 v16, 0x43800000, v16
	s_waitcnt vmcnt(6)
	v_mul_f32_e32 v1, 0x43800000, v37
	v_cvt_pk_fp8_f32 v70, v0, v1
	s_waitcnt vmcnt(5)
	v_mul_f32_e32 v4, 0x43800000, v41
	v_mul_f32_e32 v36, 0x43800000, v36
	v_cvt_pk_fp8_f32 v66, v28, v36
	s_waitcnt vmcnt(4)
	v_mul_f32_e32 v5, 0x43800000, v53
	s_waitcnt vmcnt(3)
	v_mul_f32_e32 v0, 0x43800000, v45
	v_cvt_pk_fp8_f32 v70, v4, v5 op_sel:[0,0,1]
	s_waitcnt vmcnt(2)
	v_mul_f32_e32 v1, 0x43800000, v57
	v_cvt_pk_fp8_f32 v71, v0, v1
	s_waitcnt vmcnt(1)
	v_mul_f32_e32 v0, 0x43800000, v49
	v_mul_f32_e32 v5, 0x43800000, v14
	v_mul_f32_e32 v4, 0x43800000, v22
	v_mul_f32_e32 v44, 0x43800000, v44
	v_mul_f32_e32 v56, 0x43800000, v56
	s_waitcnt vmcnt(0)
; #define LAS __attribute__((address_space(3)))
; __device__ __forceinline__ unsigned pk4_fp8(float x0, float x1, float x2, float x3) { int w = 0; w = __builtin_amdgcn_cvt_pk_fp8_f32(x0, x1, w, false); w = __builtin_amdgcn_cvt_pk_fp8_f32(x2, x3, w, true); return (unsigned)w; }
; __device__ __forceinline__ void transpose_item_fp8w(const float* W, int K, int N, unsigned char* WT, float q, LAS unsigned char* scr, int item, int lane) {
;     ...
;     for (int b = 0; b < 2; ++b) {
;         f32x4 x[16];
; #pragma unroll
;         for (int s_ = 0; s_ < 16; ++s_) x[s_] = *(const f32x4*)(src + (size_t)(32 * b + s_) * N);
; #pragma unroll
;         for (int i = 0; i < 4; ++i) {
;             u32x4 o;
;             o.x = pk4_fp8(x[0][i] * q, x[1][i] * q, x[2][i] * q, x[3][i] * q); o.y = pk4_fp8(x[4][i] * q, x[5][i] * q, x[6][i] * q, x[7][i] * q);
;             o.z = pk4_fp8(x[8][i] * q, x[9][i] * q, x[10][i] * q, x[11][i] * q); o.w = pk4_fp8(x[12][i] * q, x[13][i] * q, x[14][i] * q, x[15][i] * q);
;             *(LAS u32x4*)(scr + (l5 + 32 * i) * 80 + (2 * b + h) * 16) = o; }
	v_mul_f32_e32 v1, 0x43800000, v61
	v_cvt_pk_fp8_f32 v71, v0, v1 op_sel:[0,0,1]
	v_mul_f32_e32 v0, 0x43800000, v2
	v_mul_f32_e32 v1, 0x43800000, v6
	v_cvt_pk_fp8_f32 v136, v0, v1
	v_add_co_u32_e32 v0, vcc, s25, v80
	v_mul_f32_e32 v2, 0x43800000, v10
	s_nop 0
	v_addc_co_u32_e32 v1, vcc, 0, v81, vcc
	global_load_dwordx4 v[88:91], v[0:1], off offset:-4096 nt
	global_load_dwordx4 v[92:95], v[0:1], off nt
	v_add_co_u32_e32 v0, vcc, s26, v80
	v_cvt_pk_fp8_f32 v136, v2, v4 op_sel:[0,0,1]
	s_nop 0
	v_addc_co_u32_e32 v1, vcc, 0, v81, vcc
	global_load_dwordx4 v[128:131], v[0:1], off offset:-4096 nt
	global_load_dwordx4 v[132:135], v[0:1], off nt
	v_add_co_u32_e32 v0, vcc, s27, v80
	v_mul_f32_e32 v2, 0x43800000, v42
	s_nop 0
	v_addc_co_u32_e32 v1, vcc, 0, v81, vcc
	global_load_dwordx4 v[112:115], v[0:1], off offset:-4096 nt
	global_load_dwordx4 v[116:119], v[0:1], off nt
	v_add_co_u32_e32 v0, vcc, s28, v80
	v_mul_f32_e32 v4, 0x43800000, v54
	s_nop 0
	v_addc_co_u32_e32 v1, vcc, 0, v81, vcc
	global_load_dwordx4 v[96:99], v[0:1], off offset:-4096 nt
	global_load_dwordx4 v[100:103], v[0:1], off nt
	v_add_co_u32_e32 v0, vcc, s29, v80
	v_cvt_pk_fp8_f32 v67, v44, v56
	s_nop 0
	v_addc_co_u32_e32 v1, vcc, 0, v81, vcc
	global_load_dwordx4 v[72:75], v[0:1], off offset:-4096 nt
	global_load_dwordx4 v[76:79], v[0:1], off nt
	v_add_co_u32_e32 v0, vcc, s30, v80
	v_mul_f32_e32 v32, 0x43800000, v32
	s_nop 0
	v_addc_co_u32_e32 v1, vcc, 0, v81, vcc
	global_load_dwordx4 v[120:123], v[0:1], off offset:-4096 nt
	global_load_dwordx4 v[124:127], v[0:1], off nt
	v_add_co_u32_e32 v0, vcc, s31, v80
	v_mul_f32_e32 v40, 0x43800000, v40
	s_nop 0
	v_addc_co_u32_e32 v1, vcc, 0, v81, vcc
	global_load_dwordx4 v[104:107], v[0:1], off offset:-4096 nt
	global_load_dwordx4 v[108:111], v[0:1], off nt
	v_add_co_u32_e32 v0, vcc, s33, v80
	v_mul_f32_e32 v52, 0x43800000, v52
	s_nop 0
	v_addc_co_u32_e32 v1, vcc, 0, v81, vcc
	global_load_dwordx4 v[80:83], v[0:1], off offset:-4096 nt
	global_load_dwordx4 v[84:87], v[0:1], off nt
	v_mul_f32_e32 v0, 0x43800000, v26
	v_cvt_pk_fp8_f32 v137, v5, v0
	v_mul_f32_e32 v0, 0x43800000, v18
	v_mul_f32_e32 v1, 0x43800000, v34
	v_mul_f32_e32 v5, 0x43800000, v27
	v_cvt_pk_fp8_f32 v137, v0, v1 op_sel:[0,0,1]
	v_mul_f32_e32 v0, 0x43800000, v30
	v_mul_f32_e32 v1, 0x43800000, v38
	v_cvt_pk_fp8_f32 v138, v0, v1
	v_mul_f32_e32 v0, 0x43800000, v46
	v_mul_f32_e32 v1, 0x43800000, v58
	v_cvt_pk_fp8_f32 v139, v0, v1
	v_mul_f32_e32 v0, 0x43800000, v50
	v_mul_f32_e32 v1, 0x43800000, v62
	v_cvt_pk_fp8_f32 v138, v2, v4 op_sel:[0,0,1]
	v_cvt_pk_fp8_f32 v139, v0, v1 op_sel:[0,0,1]
	v_mul_f32_e32 v1, 0x43800000, v3
	v_mul_f32_e32 v2, 0x43800000, v7
	v_mov_b32_e32 v0, v143
	v_cvt_pk_fp8_f32 v0, v1, v2
	v_mul_f32_e32 v2, 0x43800000, v15
	v_mov_b32_e32 v1, v143
	v_cvt_pk_fp8_f32 v1, v2, v5
	v_mul_f32_e32 v3, 0x43800000, v11
	v_mul_f32_e32 v4, 0x43800000, v23
	v_cvt_pk_fp8_f32 v0, v3, v4 op_sel:[0,0,1]
	v_mul_f32_e32 v2, 0x43800000, v19
	v_mul_f32_e32 v3, 0x43800000, v35
	v_cvt_pk_fp8_f32 v1, v2, v3 op_sel:[0,0,1]
	v_mul_f32_e32 v3, 0x43800000, v31
	v_mul_f32_e32 v4, 0x43800000, v39
	v_mov_b32_e32 v2, v143
	v_cvt_pk_fp8_f32 v2, v3, v4
	v_mul_f32_e32 v4, 0x43800000, v47
	v_mul_f32_e32 v7, 0x43800000, v59
	v_mov_b32_e32 v3, v143
	v_mul_f32_e32 v48, 0x43800000, v48
	v_mul_f32_e32 v60, 0x43800000, v60
	v_cvt_pk_fp8_f32 v3, v4, v7
	v_cvt_pk_fp8_f32 v64, v8, v20 op_sel:[0,0,1]
	v_cvt_pk_fp8_f32 v65, v16, v32 op_sel:[0,0,1]
	v_cvt_pk_fp8_f32 v66, v40, v52 op_sel:[0,0,1]
	v_cvt_pk_fp8_f32 v67, v48, v60 op_sel:[0,0,1]
	v_cvt_pk_fp8_f32 v68, v9, v21 op_sel:[0,0,1]
	v_mul_f32_e32 v5, 0x43800000, v43
	v_mul_f32_e32 v6, 0x43800000, v55
	v_cvt_pk_fp8_f32 v2, v5, v6 op_sel:[0,0,1]
	v_mul_f32_e32 v4, 0x43800000, v51
	v_mul_f32_e32 v5, 0x43800000, v63
	v_cvt_pk_fp8_f32 v3, v4, v5 op_sel:[0,0,1]
	ds_write_b128 v194, v[64:67]
	ds_write_b128 v194, v[68:71] offset:2560
	ds_write_b128 v194, v[136:139] offset:5120
	ds_write_b128 v194, v[0:3] offset:7680
	s_waitcnt vmcnt(15)
	v_mul_f32_e32 v1, 0x43800000, v88
	s_waitcnt vmcnt(14)
	v_mul_f32_e32 v2, 0x43800000, v92
	v_mov_b32_e32 v0, v143
	v_cvt_pk_fp8_f32 v0, v1, v2
	s_waitcnt vmcnt(11)
	v_mul_f32_e32 v2, 0x43800000, v112
	s_waitcnt vmcnt(10)
	v_mul_f32_e32 v5, 0x43800000, v116
	v_mov_b32_e32 v1, v143
	v_cvt_pk_fp8_f32 v1, v2, v5
	v_mul_f32_e32 v3, 0x43800000, v128
	v_mul_f32_e32 v4, 0x43800000, v132
	v_cvt_pk_fp8_f32 v0, v3, v4 op_sel:[0,0,1]
	s_waitcnt vmcnt(9)
	v_mul_f32_e32 v2, 0x43800000, v96
	s_waitcnt vmcnt(8)
	v_mul_f32_e32 v3, 0x43800000, v100
	v_cvt_pk_fp8_f32 v1, v2, v3 op_sel:[0,0,1]
	s_waitcnt vmcnt(7)
	v_mul_f32_e32 v3, 0x43800000, v72
	s_waitcnt vmcnt(6)
	v_mul_f32_e32 v4, 0x43800000, v76
	v_mov_b32_e32 v2, v143
	v_cvt_pk_fp8_f32 v2, v3, v4
	v_mov_b32_e32 v3, v143
	s_waitcnt vmcnt(5)
	v_mul_f32_e32 v5, 0x43800000, v120
	s_waitcnt vmcnt(4)
	v_mul_f32_e32 v6, 0x43800000, v124
	s_waitcnt vmcnt(3)
	v_mul_f32_e32 v4, 0x43800000, v104
	s_waitcnt vmcnt(2)
	v_mul_f32_e32 v7, 0x43800000, v108
	v_cvt_pk_fp8_f32 v3, v4, v7
	v_cvt_pk_fp8_f32 v2, v5, v6 op_sel:[0,0,1]
	v_mul_f32_e32 v6, 0x43800000, v93
	v_mul_f32_e32 v9, 0x43800000, v117
	s_waitcnt vmcnt(1)
	v_mul_f32_e32 v4, 0x43800000, v80
	s_waitcnt vmcnt(0)
; #define LAS __attribute__((address_space(3)))
; __device__ __forceinline__ unsigned pk4_fp8(float x0, float x1, float x2, float x3) { int w = 0; w = __builtin_amdgcn_cvt_pk_fp8_f32(x0, x1, w, false); w = __builtin_amdgcn_cvt_pk_fp8_f32(x2, x3, w, true); return (unsigned)w; }
; __device__ __forceinline__ void transpose_item_fp8w(const float* W, int K, int N, unsigned char* WT, float q, LAS unsigned char* scr, int item, int lane) {
;     ...
; #pragma unroll
;         for (int i = 0; i < 4; ++i) {
;             u32x4 o;
;             o.x = pk4_fp8(x[0][i] * q, x[1][i] * q, x[2][i] * q, x[3][i] * q); o.y = pk4_fp8(x[4][i] * q, x[5][i] * q, x[6][i] * q, x[7][i] * q);
;             o.z = pk4_fp8(x[8][i] * q, x[9][i] * q, x[10][i] * q, x[11][i] * q); o.w = pk4_fp8(x[12][i] * q, x[13][i] * q, x[14][i] * q, x[15][i] * q);
;             *(LAS u32x4*)(scr + (l5 + 32 * i) * 80 + (2 * b + h) * 16) = o; }
;     }
;     asm volatile("s_waitcnt lgkmcnt(0)" ::: "memory");
; #pragma unroll
;     for (int qd = 0; qd < 8; ++qd) {
;         const int rho = 16 * qd + (lane >> 2), piece = lane & 3;
;         const u32x4 o = *(const LAS u32x4*)(scr + rho * 80 + piece * 16);
;         const int nl = 4 * (rho & 31) + (rho >> 5);
;         *(u32x4*)(WT + (size_t)(n0 + nl) * K + k0 + piece * 16) = o; }
;     asm volatile("s_waitcnt lgkmcnt(0)" ::: "memory");
	v_mul_f32_e32 v5, 0x43800000, v84
	v_cvt_pk_fp8_f32 v3, v4, v5 op_sel:[0,0,1]
	v_mul_f32_e32 v5, 0x43800000, v89
	v_mov_b32_e32 v4, v143
	v_cvt_pk_fp8_f32 v4, v5, v6
	v_mul_f32_e32 v6, 0x43800000, v113
	v_mov_b32_e32 v5, v143
	v_cvt_pk_fp8_f32 v5, v6, v9
	v_mul_f32_e32 v7, 0x43800000, v129
	v_mul_f32_e32 v8, 0x43800000, v133
	v_cvt_pk_fp8_f32 v4, v7, v8 op_sel:[0,0,1]
	v_mul_f32_e32 v6, 0x43800000, v97
	v_mul_f32_e32 v7, 0x43800000, v101
	v_cvt_pk_fp8_f32 v5, v6, v7 op_sel:[0,0,1]
	v_mul_f32_e32 v7, 0x43800000, v73
	v_mul_f32_e32 v8, 0x43800000, v77
	v_mov_b32_e32 v6, v143
	v_cvt_pk_fp8_f32 v6, v7, v8
	v_mul_f32_e32 v8, 0x43800000, v105
	v_mul_f32_e32 v11, 0x43800000, v109
	v_mov_b32_e32 v7, v143
	v_cvt_pk_fp8_f32 v7, v8, v11
	v_mul_f32_e32 v9, 0x43800000, v121
	v_mul_f32_e32 v10, 0x43800000, v125
	v_cvt_pk_fp8_f32 v6, v9, v10 op_sel:[0,0,1]
	v_mul_f32_e32 v8, 0x43800000, v81
	v_mul_f32_e32 v9, 0x43800000, v85
	v_cvt_pk_fp8_f32 v7, v8, v9 op_sel:[0,0,1]
	v_mul_f32_e32 v9, 0x43800000, v90
	v_mul_f32_e32 v10, 0x43800000, v94
	v_mov_b32_e32 v8, v143
	v_cvt_pk_fp8_f32 v8, v9, v10
	v_mul_f32_e32 v10, 0x43800000, v114
	v_mul_f32_e32 v13, 0x43800000, v118
	v_mov_b32_e32 v9, v143
	v_cvt_pk_fp8_f32 v9, v10, v13
	v_mul_f32_e32 v11, 0x43800000, v130
	v_mul_f32_e32 v12, 0x43800000, v134
	v_cvt_pk_fp8_f32 v8, v11, v12 op_sel:[0,0,1]
	v_mul_f32_e32 v10, 0x43800000, v98
	v_mul_f32_e32 v11, 0x43800000, v102
	v_cvt_pk_fp8_f32 v9, v10, v11 op_sel:[0,0,1]
	v_mul_f32_e32 v11, 0x43800000, v74
	v_mul_f32_e32 v12, 0x43800000, v78
	v_mov_b32_e32 v10, v143
	v_cvt_pk_fp8_f32 v10, v11, v12
	v_mul_f32_e32 v12, 0x43800000, v106
	v_mul_f32_e32 v15, 0x43800000, v110
	v_mov_b32_e32 v11, v143
	v_cvt_pk_fp8_f32 v11, v12, v15
	v_mul_f32_e32 v13, 0x43800000, v122
	v_mul_f32_e32 v14, 0x43800000, v126
	v_cvt_pk_fp8_f32 v10, v13, v14 op_sel:[0,0,1]
	v_mul_f32_e32 v12, 0x43800000, v82
	v_mul_f32_e32 v13, 0x43800000, v86
	v_cvt_pk_fp8_f32 v11, v12, v13 op_sel:[0,0,1]
	v_mul_f32_e32 v13, 0x43800000, v91
	v_mul_f32_e32 v14, 0x43800000, v95
	v_mov_b32_e32 v12, v143
	v_cvt_pk_fp8_f32 v12, v13, v14
	v_mul_f32_e32 v14, 0x43800000, v115
	v_mul_f32_e32 v17, 0x43800000, v119
	v_mov_b32_e32 v13, v143
	v_cvt_pk_fp8_f32 v13, v14, v17
	v_mul_f32_e32 v15, 0x43800000, v131
	v_mul_f32_e32 v16, 0x43800000, v135
	v_cvt_pk_fp8_f32 v12, v15, v16 op_sel:[0,0,1]
	v_mul_f32_e32 v14, 0x43800000, v99
	v_mul_f32_e32 v15, 0x43800000, v103
	v_cvt_pk_fp8_f32 v13, v14, v15 op_sel:[0,0,1]
	v_mul_f32_e32 v15, 0x43800000, v75
	v_mul_f32_e32 v16, 0x43800000, v79
	v_mov_b32_e32 v14, v143
	v_cvt_pk_fp8_f32 v14, v15, v16
	v_mul_f32_e32 v16, 0x43800000, v107
	v_mul_f32_e32 v19, 0x43800000, v111
	v_mov_b32_e32 v15, v143
	v_cvt_pk_fp8_f32 v15, v16, v19
	v_mul_f32_e32 v17, 0x43800000, v123
	v_mul_f32_e32 v18, 0x43800000, v127
	v_cvt_pk_fp8_f32 v14, v17, v18 op_sel:[0,0,1]
	v_mul_f32_e32 v16, 0x43800000, v83
	v_mul_f32_e32 v17, 0x43800000, v87
	v_cvt_pk_fp8_f32 v15, v16, v17 op_sel:[0,0,1]
	ds_write_b128 v194, v[0:3] offset:32
	ds_write_b128 v194, v[4:7] offset:2592
	ds_write_b128 v194, v[8:11] offset:5152
	ds_write_b128 v194, v[12:15] offset:7712
	s_waitcnt lgkmcnt(0)
	ds_read_b128 v[0:3], v195
	v_add_u32_e32 v4, s6, v181
	v_ashrrev_i32_e32 v5, 31, v4
	v_lshl_add_u64 v[8:9], s[68:69], 0, v[144:145]
	v_lshlrev_b64 v[4:5], 10, v[4:5]
	v_lshl_add_u64 v[10:11], v[8:9], 0, v[4:5]
	ds_read_b128 v[4:7], v195 offset:1280
	s_waitcnt lgkmcnt(1)
	global_store_dwordx4 v[10:11], v[0:3], off nt
	s_nop 1
	v_add_u32_e32 v0, s6, v182
	v_ashrrev_i32_e32 v1, 31, v0
	v_lshlrev_b64 v[0:1], 10, v[0:1]
	v_lshl_add_u64 v[0:1], v[8:9], 0, v[0:1]
	s_waitcnt lgkmcnt(0)
	global_store_dwordx4 v[0:1], v[4:7], off nt
	ds_read_b128 v[0:3], v195 offset:2560
	s_nop 0
	v_add_u32_e32 v4, s6, v183
	v_ashrrev_i32_e32 v5, 31, v4
	v_lshlrev_b64 v[4:5], 10, v[4:5]
	v_lshl_add_u64 v[10:11], v[8:9], 0, v[4:5]
	ds_read_b128 v[4:7], v195 offset:3840
	s_waitcnt lgkmcnt(1)
	global_store_dwordx4 v[10:11], v[0:3], off nt
	s_nop 1
	v_add_u32_e32 v0, s6, v184
	v_ashrrev_i32_e32 v1, 31, v0
	v_lshlrev_b64 v[0:1], 10, v[0:1]
	v_lshl_add_u64 v[0:1], v[8:9], 0, v[0:1]
	s_waitcnt lgkmcnt(0)
	global_store_dwordx4 v[0:1], v[4:7], off nt
	ds_read_b128 v[0:3], v195 offset:5120
	s_nop 0
	v_add_u32_e32 v4, s6, v185
	v_ashrrev_i32_e32 v5, 31, v4
	v_lshlrev_b64 v[4:5], 10, v[4:5]
	v_lshl_add_u64 v[10:11], v[8:9], 0, v[4:5]
	ds_read_b128 v[4:7], v195 offset:6400
	s_waitcnt lgkmcnt(1)
	global_store_dwordx4 v[10:11], v[0:3], off nt
	s_nop 1
	v_add_u32_e32 v0, s6, v186
	v_ashrrev_i32_e32 v1, 31, v0
	v_lshlrev_b64 v[0:1], 10, v[0:1]
	v_lshl_add_u64 v[0:1], v[8:9], 0, v[0:1]
	s_waitcnt lgkmcnt(0)
	global_store_dwordx4 v[0:1], v[4:7], off nt
	ds_read_b128 v[0:3], v195 offset:7680
	s_nop 0
	v_add_u32_e32 v4, s6, v187
	v_ashrrev_i32_e32 v5, 31, v4
	v_lshlrev_b64 v[4:5], 10, v[4:5]
	v_lshl_add_u64 v[10:11], v[8:9], 0, v[4:5]
	ds_read_b128 v[4:7], v195 offset:8960
	s_waitcnt lgkmcnt(1)
	global_store_dwordx4 v[10:11], v[0:3], off nt
	s_nop 1
	v_add_u32_e32 v0, s6, v188
	v_ashrrev_i32_e32 v1, 31, v0
	v_lshlrev_b64 v[0:1], 10, v[0:1]
	v_lshl_add_u64 v[0:1], v[8:9], 0, v[0:1]
	s_waitcnt lgkmcnt(0)
	global_store_dwordx4 v[0:1], v[4:7], off nt
	s_waitcnt lgkmcnt(0)
	s_mov_b64 s[6:7], 0
; __device__ __forceinline__ unsigned pk4_fp8(float x0, float x1, float x2, float x3) { int w = 0; w = __builtin_amdgcn_cvt_pk_fp8_f32(x0, x1, w, false); w = __builtin_amdgcn_cvt_pk_fp8_f32(x2, x3, w, true); return (unsigned)w; }
; __device__ __forceinline__ void transpose_item_fp8w(const float* W, int K, int N, unsigned char* WT, float q, LAS unsigned char* scr, int item, int lane) {
;     const int nblk = N / 128, kb = item / nblk, nb = item % nblk, k0 = 64 * kb, n0 = 128 * nb;
;     const int l5 = lane & 31, h = lane >> 5;
;     const float* src = W + (size_t)(k0 + 16 * h) * N + n0 + 4 * l5;
; #pragma unroll
;     for (int b = 0; b < 2; ++b) {
;         f32x4 x[16];
; #pragma unroll
;         for (int s_ = 0; s_ < 16; ++s_) x[s_] = *(const f32x4*)(src + (size_t)(32 * b + s_) * N);
; #pragma unroll
;         for (int i = 0; i < 4; ++i) {
;             u32x4 o;
;             o.x = pk4_fp8(x[0][i] * q, x[1][i] * q, x[2][i] * q, x[3][i] * q); o.y = pk4_fp8(x[4][i] * q, x[5][i] * q, x[6][i] * q, x[7][i] * q);
.LBB0_44:
	s_andn2_b64 vcc, exec, s[6:7]
	s_cbranch_vccnz .LBB0_46
	s_add_i32 s67, s66, 0xfffff910
	s_lshr_b32 s4, s67, 8
	s_lshl_b64 s[6:7], s[4:5], 23
	s_add_u32 s68, s18, s6
	s_addc_u32 s69, s19, s7
	s_lshl_b64 s[8:9], s[4:5], 21
	v_readlane_b32 s4, v246, 15
	s_add_u32 s7, s4, s8
	v_readlane_b32 s4, v246, 16
	s_addc_u32 s8, s4, s9
	s_lshl_b32 s4, s67, 6
	s_and_b32 s9, s4, 0x3c0
	v_add_u32_e32 v0, s9, v177
	s_lshl_b32 s4, s67, 3
	v_ashrrev_i32_e32 v1, 31, v0
	s_and_b32 s6, s4, 0x780
	v_lshlrev_b64 v[0:1], 13, v[0:1]
	v_lshl_add_u64 v[0:1], s[68:69], 0, v[0:1]
	s_lshl_b32 s4, s6, 2
	v_lshl_add_u64 v[0:1], v[0:1], 0, s[4:5]
	v_lshl_add_u64 v[128:129], v[0:1], 0, v[142:143]
	v_add_co_u32_e32 v4, vcc, s10, v128
	v_mov_b32_e32 v64, v143
	s_nop 0
	v_addc_co_u32_e32 v5, vcc, 0, v129, vcc
	v_add_co_u32_e32 v8, vcc, s11, v128
	global_load_dwordx4 v[0:3], v[128:129], off nt
	s_nop 0
	global_load_dwordx4 v[4:7], v[4:5], off nt
	v_addc_co_u32_e32 v9, vcc, 0, v129, vcc
	v_add_co_u32_e32 v12, vcc, s15, v128
	v_mov_b32_e32 v65, v143
	s_nop 0
	v_addc_co_u32_e32 v13, vcc, 0, v129, vcc
	v_add_co_u32_e32 v16, vcc, s20, v128
	global_load_dwordx4 v[8:11], v[8:9], off nt
	s_nop 0
	global_load_dwordx4 v[12:15], v[12:13], off nt
	v_addc_co_u32_e32 v17, vcc, 0, v129, vcc
	v_add_co_u32_e32 v20, vcc, s21, v128
	v_mov_b32_e32 v66, v143
	s_nop 0
	v_addc_co_u32_e32 v21, vcc, 0, v129, vcc
	v_add_co_u32_e32 v24, vcc, s22, v128
	global_load_dwordx4 v[16:19], v[16:17], off nt
	s_nop 0
	global_load_dwordx4 v[20:23], v[20:21], off nt
	v_addc_co_u32_e32 v25, vcc, 0, v129, vcc
	v_add_co_u32_e32 v28, vcc, s23, v128
	v_mov_b32_e32 v67, v143
	s_nop 0
	v_addc_co_u32_e32 v29, vcc, 0, v129, vcc
	v_add_co_u32_e32 v32, vcc, s34, v128
	global_load_dwordx4 v[24:27], v[24:25], off nt
	s_nop 0
	global_load_dwordx4 v[28:31], v[28:29], off nt
	v_addc_co_u32_e32 v33, vcc, 0, v129, vcc
	v_add_co_u32_e32 v36, vcc, s35, v128
	v_mov_b32_e32 v96, v143
	s_nop 0
	v_addc_co_u32_e32 v37, vcc, 0, v129, vcc
	v_add_co_u32_e32 v40, vcc, s36, v128
	global_load_dwordx4 v[32:35], v[32:33], off nt
	s_nop 0
	global_load_dwordx4 v[36:39], v[36:37], off nt
	v_addc_co_u32_e32 v41, vcc, 0, v129, vcc
	v_add_co_u32_e32 v44, vcc, s37, v128
	v_mov_b32_e32 v97, v143
	s_nop 0
	v_addc_co_u32_e32 v45, vcc, 0, v129, vcc
	v_add_co_u32_e32 v48, vcc, s38, v128
	global_load_dwordx4 v[40:43], v[40:41], off nt
	s_nop 0
	global_load_dwordx4 v[44:47], v[44:45], off nt
	v_addc_co_u32_e32 v49, vcc, 0, v129, vcc
	v_add_co_u32_e32 v52, vcc, s39, v128
	v_mov_b32_e32 v98, v143
	s_nop 0
	v_addc_co_u32_e32 v53, vcc, 0, v129, vcc
	global_load_dwordx4 v[48:51], v[48:49], off nt
	s_nop 0
	global_load_dwordx4 v[52:55], v[52:53], off nt
	v_add_co_u32_e32 v56, vcc, s40, v128
	v_mov_b32_e32 v99, v143
	s_nop 0
	v_addc_co_u32_e32 v57, vcc, 0, v129, vcc
	v_add_co_u32_e32 v60, vcc, s41, v128
	v_mov_b32_e32 v136, v143
	s_nop 0
	v_addc_co_u32_e32 v61, vcc, 0, v129, vcc
	global_load_dwordx4 v[56:59], v[56:57], off nt
	s_nop 0
	global_load_dwordx4 v[60:63], v[60:61], off nt
	v_mov_b32_e32 v137, v143
	v_mov_b32_e32 v138, v143
	v_mov_b32_e32 v139, v143
	s_add_u32 s68, s7, s9
	s_addc_u32 s69, s8, 0
	s_waitcnt vmcnt(15)
	v_mul_f32_e32 v0, 0x43000000, v0
	s_waitcnt vmcnt(14)
	v_mul_f32_e32 v4, 0x43000000, v4
	v_cvt_pk_fp8_f32 v64, v0, v4
	s_waitcnt vmcnt(13)
	v_mul_f32_e32 v8, 0x43000000, v8
	s_waitcnt vmcnt(12)
	v_mul_f32_e32 v12, 0x43000000, v12
	v_cvt_pk_fp8_f32 v64, v8, v12 op_sel:[0,0,1]
	s_waitcnt vmcnt(11)
	v_mul_f32_e32 v0, 0x43000000, v16
	s_waitcnt vmcnt(10)
	v_mul_f32_e32 v4, 0x43000000, v20
	v_cvt_pk_fp8_f32 v65, v0, v4
	s_waitcnt vmcnt(9)
	v_mul_f32_e32 v0, 0x43000000, v24
	s_waitcnt vmcnt(8)
	v_mul_f32_e32 v4, 0x43000000, v28
	v_cvt_pk_fp8_f32 v65, v0, v4 op_sel:[0,0,1]
	s_waitcnt vmcnt(7)
	v_mul_f32_e32 v0, 0x43000000, v32
	s_waitcnt vmcnt(6)
	v_mul_f32_e32 v4, 0x43000000, v36
	v_cvt_pk_fp8_f32 v66, v0, v4
	s_waitcnt vmcnt(5)
	v_mul_f32_e32 v8, 0x43000000, v40
	s_waitcnt vmcnt(4)
	v_mul_f32_e32 v12, 0x43000000, v44
	v_cvt_pk_fp8_f32 v66, v8, v12 op_sel:[0,0,1]
	v_mul_f32_e32 v8, 0x43000000, v18
	s_waitcnt vmcnt(3)
	v_mul_f32_e32 v0, 0x43000000, v48
	s_waitcnt vmcnt(2)
	v_mul_f32_e32 v4, 0x43000000, v52
	v_cvt_pk_fp8_f32 v67, v0, v4
	s_waitcnt vmcnt(1)
	v_mul_f32_e32 v0, 0x43000000, v56
	s_waitcnt vmcnt(0)
	v_mul_f32_e32 v4, 0x43000000, v60
	v_cvt_pk_fp8_f32 v67, v0, v4 op_sel:[0,0,1]
	v_mul_f32_e32 v0, 0x43000000, v1
	v_mul_f32_e32 v1, 0x43000000, v5
	v_cvt_pk_fp8_f32 v96, v0, v1
	v_mul_f32_e32 v0, 0x43000000, v17
	v_mul_f32_e32 v1, 0x43000000, v21
	v_cvt_pk_fp8_f32 v97, v0, v1
	v_mul_f32_e32 v0, 0x43000000, v25
	v_mul_f32_e32 v1, 0x43000000, v29
	v_mul_f32_e32 v4, 0x43000000, v9
	v_cvt_pk_fp8_f32 v97, v0, v1 op_sel:[0,0,1]
	v_mul_f32_e32 v0, 0x43000000, v33
	v_mul_f32_e32 v1, 0x43000000, v37
	v_cvt_pk_fp8_f32 v98, v0, v1
	v_mul_f32_e32 v0, 0x43000000, v49
	v_mul_f32_e32 v1, 0x43000000, v53
	v_cvt_pk_fp8_f32 v99, v0, v1
	v_mul_f32_e32 v0, 0x43000000, v57
	v_mul_f32_e32 v1, 0x43000000, v61
	v_mul_f32_e32 v5, 0x43000000, v13
	v_cvt_pk_fp8_f32 v99, v0, v1 op_sel:[0,0,1]
	v_mul_f32_e32 v0, 0x43000000, v2
	v_mul_f32_e32 v1, 0x43000000, v6
	v_cvt_pk_fp8_f32 v136, v0, v1
	v_add_co_u32_e32 v0, vcc, s42, v128
	v_cvt_pk_fp8_f32 v96, v4, v5 op_sel:[0,0,1]
	v_mul_f32_e32 v4, 0x43000000, v41
	v_mul_f32_e32 v5, 0x43000000, v45
	v_addc_co_u32_e32 v1, vcc, 0, v129, vcc
	v_cvt_pk_fp8_f32 v98, v4, v5 op_sel:[0,0,1]
	v_add_co_u32_e32 v4, vcc, s43, v128
	v_mul_f32_e32 v2, 0x43000000, v10
	s_nop 0
	v_addc_co_u32_e32 v5, vcc, 0, v129, vcc
	global_load_dwordx4 v[68:71], v[0:1], off nt
	global_load_dwordx4 v[72:75], v[4:5], off nt
	v_add_co_u32_e32 v0, vcc, s44, v128
	v_mul_f32_e32 v6, 0x43000000, v14
	s_nop 0
	v_addc_co_u32_e32 v1, vcc, 0, v129, vcc
	v_add_co_u32_e32 v4, vcc, s45, v128
	v_cvt_pk_fp8_f32 v136, v2, v6 op_sel:[0,0,1]
	s_nop 0
	v_addc_co_u32_e32 v5, vcc, 0, v129, vcc
	global_load_dwordx4 v[76:79], v[0:1], off nt
	global_load_dwordx4 v[80:83], v[4:5], off nt
	v_add_co_u32_e32 v0, vcc, s46, v128
	v_mul_f32_e32 v2, 0x43000000, v42
	s_nop 0
	v_addc_co_u32_e32 v1, vcc, 0, v129, vcc
	v_add_co_u32_e32 v4, vcc, s47, v128
	v_mul_f32_e32 v6, 0x43000000, v47
	s_nop 0
	v_addc_co_u32_e32 v5, vcc, 0, v129, vcc
	global_load_dwordx4 v[84:87], v[0:1], off nt
	global_load_dwordx4 v[88:91], v[4:5], off nt
	v_add_co_u32_e32 v0, vcc, s48, v128
	s_waitcnt vmcnt(2)
; #define LAS __attribute__((address_space(3)))
; __device__ __forceinline__ unsigned pk4_fp8(float x0, float x1, float x2, float x3) { int w = 0; w = __builtin_amdgcn_cvt_pk_fp8_f32(x0, x1, w, false); w = __builtin_amdgcn_cvt_pk_fp8_f32(x2, x3, w, true); return (unsigned)w; }
; __device__ __forceinline__ void transpose_item_fp8w(const float* W, int K, int N, unsigned char* WT, float q, LAS unsigned char* scr, int item, int lane) {
;     ...
;     for (int b = 0; b < 2; ++b) {
;         f32x4 x[16];
; #pragma unroll
;         for (int s_ = 0; s_ < 16; ++s_) x[s_] = *(const f32x4*)(src + (size_t)(32 * b + s_) * N);
; #pragma unroll
;         for (int i = 0; i < 4; ++i) {
;             u32x4 o;
;             o.x = pk4_fp8(x[0][i] * q, x[1][i] * q, x[2][i] * q, x[3][i] * q); o.y = pk4_fp8(x[4][i] * q, x[5][i] * q, x[6][i] * q, x[7][i] * q);
;             o.z = pk4_fp8(x[8][i] * q, x[9][i] * q, x[10][i] * q, x[11][i] * q); o.w = pk4_fp8(x[12][i] * q, x[13][i] * q, x[14][i] * q, x[15][i] * q);
;             *(LAS u32x4*)(scr + (l5 + 32 * i) * 80 + (2 * b + h) * 16) = o; }
	v_mul_f32_e32 v12, 0x43000000, v82
	v_addc_co_u32_e32 v1, vcc, 0, v129, vcc
	v_add_co_u32_e32 v4, vcc, s49, v128
	v_mul_f32_e32 v16, 0x43000000, v83
	s_nop 0
	v_addc_co_u32_e32 v5, vcc, 0, v129, vcc
	global_load_dwordx4 v[92:95], v[0:1], off nt
	global_load_dwordx4 v[100:103], v[4:5], off nt
	v_add_co_u32_e32 v0, vcc, s50, v128
	s_waitcnt vmcnt(2)
	v_mul_f32_e32 v9, 0x43000000, v89
	v_addc_co_u32_e32 v1, vcc, 0, v129, vcc
	v_add_co_u32_e32 v4, vcc, s51, v128
	v_mul_f32_e32 v13, 0x43000000, v90
	s_nop 0
	v_addc_co_u32_e32 v5, vcc, 0, v129, vcc
	global_load_dwordx4 v[104:107], v[0:1], off nt
	global_load_dwordx4 v[108:111], v[4:5], off nt
	v_add_co_u32_e32 v0, vcc, s52, v128
	v_mul_f32_e32 v17, 0x43000000, v91
	s_nop 0
	v_addc_co_u32_e32 v1, vcc, 0, v129, vcc
	v_add_co_u32_e32 v4, vcc, s53, v128
	s_nop 1
	v_addc_co_u32_e32 v5, vcc, 0, v129, vcc
	global_load_dwordx4 v[112:115], v[0:1], off nt
	global_load_dwordx4 v[116:119], v[4:5], off nt
	v_add_co_u32_e32 v0, vcc, s54, v128
	s_waitcnt vmcnt(0)
	v_mul_f32_e32 v10, 0x43000000, v117
	v_addc_co_u32_e32 v1, vcc, 0, v129, vcc
	v_add_co_u32_e32 v4, vcc, s55, v128
	v_mul_f32_e32 v14, 0x43000000, v118
	s_nop 0
	v_addc_co_u32_e32 v5, vcc, 0, v129, vcc
	global_load_dwordx4 v[120:123], v[0:1], off nt
	global_load_dwordx4 v[124:127], v[4:5], off nt
	v_add_co_u32_e32 v0, vcc, s56, v128
	v_mul_f32_e32 v18, 0x43000000, v119
	s_nop 0
	v_addc_co_u32_e32 v1, vcc, 0, v129, vcc
	v_add_co_u32_e32 v4, vcc, s57, v128
	s_nop 1
	v_addc_co_u32_e32 v5, vcc, 0, v129, vcc
	global_load_dwordx4 v[128:131], v[0:1], off nt
	global_load_dwordx4 v[132:135], v[4:5], off nt
	v_mul_f32_e32 v0, 0x43000000, v22
	v_cvt_pk_fp8_f32 v137, v8, v0
	v_mul_f32_e32 v0, 0x43000000, v26
	v_mul_f32_e32 v1, 0x43000000, v30
	v_mul_f32_e32 v4, 0x43000000, v46
	v_cvt_pk_fp8_f32 v137, v0, v1 op_sel:[0,0,1]
	v_mul_f32_e32 v0, 0x43000000, v34
	v_mul_f32_e32 v1, 0x43000000, v38
	v_cvt_pk_fp8_f32 v138, v0, v1
	v_mul_f32_e32 v0, 0x43000000, v50
	v_mul_f32_e32 v1, 0x43000000, v54
	v_cvt_pk_fp8_f32 v139, v0, v1
	v_mul_f32_e32 v0, 0x43000000, v58
	v_mul_f32_e32 v1, 0x43000000, v62
	v_cvt_pk_fp8_f32 v138, v2, v4 op_sel:[0,0,1]
	v_cvt_pk_fp8_f32 v139, v0, v1 op_sel:[0,0,1]
	v_mul_f32_e32 v1, 0x43000000, v3
	v_mul_f32_e32 v2, 0x43000000, v7
	v_mov_b32_e32 v0, v143
	v_cvt_pk_fp8_f32 v0, v1, v2
	v_mul_f32_e32 v2, 0x43000000, v19
	v_mul_f32_e32 v5, 0x43000000, v23
	v_mov_b32_e32 v1, v143
	v_cvt_pk_fp8_f32 v1, v2, v5
	v_mul_f32_e32 v3, 0x43000000, v11
	v_mul_f32_e32 v4, 0x43000000, v15
	v_cvt_pk_fp8_f32 v0, v3, v4 op_sel:[0,0,1]
	v_mul_f32_e32 v2, 0x43000000, v27
	v_mul_f32_e32 v3, 0x43000000, v31
	v_cvt_pk_fp8_f32 v1, v2, v3 op_sel:[0,0,1]
	v_mul_f32_e32 v3, 0x43000000, v35
	v_mul_f32_e32 v4, 0x43000000, v39
	v_mov_b32_e32 v2, v143
	v_cvt_pk_fp8_f32 v2, v3, v4
	v_mul_f32_e32 v4, 0x43000000, v51
	v_mul_f32_e32 v7, 0x43000000, v55
	v_mov_b32_e32 v3, v143
	v_cvt_pk_fp8_f32 v3, v4, v7
	v_mul_f32_e32 v5, 0x43000000, v43
	v_cvt_pk_fp8_f32 v2, v5, v6 op_sel:[0,0,1]
	v_mul_f32_e32 v4, 0x43000000, v59
	v_mul_f32_e32 v5, 0x43000000, v63
	v_cvt_pk_fp8_f32 v3, v4, v5 op_sel:[0,0,1]
	ds_write_b128 v194, v[64:67]
	ds_write_b128 v194, v[96:99] offset:2560
	ds_write_b128 v194, v[136:139] offset:5120
	ds_write_b128 v194, v[0:3] offset:7680
	v_mul_f32_e32 v1, 0x43000000, v68
	v_mul_f32_e32 v2, 0x43000000, v72
	v_mov_b32_e32 v0, v143
	v_cvt_pk_fp8_f32 v0, v1, v2
	v_mul_f32_e32 v2, 0x43000000, v84
	v_mul_f32_e32 v5, 0x43000000, v88
	v_mov_b32_e32 v1, v143
	v_cvt_pk_fp8_f32 v1, v2, v5
	v_mul_f32_e32 v3, 0x43000000, v76
	v_mul_f32_e32 v4, 0x43000000, v80
	v_cvt_pk_fp8_f32 v0, v3, v4 op_sel:[0,0,1]
	v_mul_f32_e32 v2, 0x43000000, v92
	v_mul_f32_e32 v3, 0x43000000, v100
	v_cvt_pk_fp8_f32 v1, v2, v3 op_sel:[0,0,1]
	v_mul_f32_e32 v3, 0x43000000, v104
	v_mul_f32_e32 v4, 0x43000000, v108
	v_mov_b32_e32 v2, v143
	v_cvt_pk_fp8_f32 v2, v3, v4
	v_mov_b32_e32 v3, v143
	v_mul_f32_e32 v5, 0x43000000, v112
	v_mul_f32_e32 v6, 0x43000000, v116
	v_cvt_pk_fp8_f32 v2, v5, v6 op_sel:[0,0,1]
	v_mul_f32_e32 v6, 0x43000000, v73
	s_waitcnt vmcnt(3)
	v_mul_f32_e32 v4, 0x43000000, v120
	s_waitcnt vmcnt(2)
	v_mul_f32_e32 v7, 0x43000000, v124
	v_cvt_pk_fp8_f32 v3, v4, v7
	v_mul_f32_e32 v7, 0x43000000, v77
	v_mul_f32_e32 v8, 0x43000000, v81
	v_mul_f32_e32 v11, 0x43000000, v125
	v_mul_f32_e32 v15, 0x43000000, v126
	v_mul_f32_e32 v19, 0x43000000, v127
	s_waitcnt vmcnt(1)
	v_mul_f32_e32 v4, 0x43000000, v128
	s_waitcnt vmcnt(0)
; #define LAS __attribute__((address_space(3)))
; __device__ __forceinline__ unsigned pk4_fp8(float x0, float x1, float x2, float x3) { int w = 0; w = __builtin_amdgcn_cvt_pk_fp8_f32(x0, x1, w, false); w = __builtin_amdgcn_cvt_pk_fp8_f32(x2, x3, w, true); return (unsigned)w; }
; __device__ __forceinline__ void transpose_item_fp8w(const float* W, int K, int N, unsigned char* WT, float q, LAS unsigned char* scr, int item, int lane) {
;     ...
; #pragma unroll
;         for (int i = 0; i < 4; ++i) {
;             u32x4 o;
;             o.x = pk4_fp8(x[0][i] * q, x[1][i] * q, x[2][i] * q, x[3][i] * q); o.y = pk4_fp8(x[4][i] * q, x[5][i] * q, x[6][i] * q, x[7][i] * q);
;             o.z = pk4_fp8(x[8][i] * q, x[9][i] * q, x[10][i] * q, x[11][i] * q); o.w = pk4_fp8(x[12][i] * q, x[13][i] * q, x[14][i] * q, x[15][i] * q);
;             *(LAS u32x4*)(scr + (l5 + 32 * i) * 80 + (2 * b + h) * 16) = o; }
;     }
;     asm volatile("s_waitcnt lgkmcnt(0)" ::: "memory");
; #pragma unroll
;     for (int qd = 0; qd < 8; ++qd) {
;         const int rho = 16 * qd + (lane >> 2), piece = lane & 3;
;         const u32x4 o = *(const LAS u32x4*)(scr + rho * 80 + piece * 16);
;         const int nl = 4 * (rho & 31) + (rho >> 5);
;         *(u32x4*)(WT + (size_t)(n0 + nl) * K + k0 + piece * 16) = o; }
;     asm volatile("s_waitcnt lgkmcnt(0)" ::: "memory");
	v_mul_f32_e32 v5, 0x43000000, v132
	v_cvt_pk_fp8_f32 v3, v4, v5 op_sel:[0,0,1]
	v_mul_f32_e32 v5, 0x43000000, v69
	v_mov_b32_e32 v4, v143
	v_cvt_pk_fp8_f32 v4, v5, v6
	v_mul_f32_e32 v6, 0x43000000, v85
	v_mov_b32_e32 v5, v143
	v_cvt_pk_fp8_f32 v5, v6, v9
	v_cvt_pk_fp8_f32 v4, v7, v8 op_sel:[0,0,1]
	v_mul_f32_e32 v6, 0x43000000, v93
	v_mul_f32_e32 v7, 0x43000000, v101
	v_cvt_pk_fp8_f32 v5, v6, v7 op_sel:[0,0,1]
	v_mul_f32_e32 v7, 0x43000000, v105
	v_mul_f32_e32 v8, 0x43000000, v109
	v_mov_b32_e32 v6, v143
	v_cvt_pk_fp8_f32 v6, v7, v8
	v_mul_f32_e32 v8, 0x43000000, v121
	v_mov_b32_e32 v7, v143
	v_cvt_pk_fp8_f32 v7, v8, v11
	v_mul_f32_e32 v9, 0x43000000, v113
	v_cvt_pk_fp8_f32 v6, v9, v10 op_sel:[0,0,1]
	v_mul_f32_e32 v8, 0x43000000, v129
	v_mul_f32_e32 v9, 0x43000000, v133
	v_cvt_pk_fp8_f32 v7, v8, v9 op_sel:[0,0,1]
	v_mul_f32_e32 v9, 0x43000000, v70
	v_mul_f32_e32 v10, 0x43000000, v74
	v_mov_b32_e32 v8, v143
	v_cvt_pk_fp8_f32 v8, v9, v10
	v_mul_f32_e32 v10, 0x43000000, v86
	v_mov_b32_e32 v9, v143
	v_cvt_pk_fp8_f32 v9, v10, v13
	v_mul_f32_e32 v11, 0x43000000, v78
	v_cvt_pk_fp8_f32 v8, v11, v12 op_sel:[0,0,1]
	v_mul_f32_e32 v10, 0x43000000, v94
	v_mul_f32_e32 v11, 0x43000000, v102
	v_cvt_pk_fp8_f32 v9, v10, v11 op_sel:[0,0,1]
	v_mul_f32_e32 v11, 0x43000000, v106
	v_mul_f32_e32 v12, 0x43000000, v110
	v_mov_b32_e32 v10, v143
	v_cvt_pk_fp8_f32 v10, v11, v12
	v_mul_f32_e32 v12, 0x43000000, v122
	v_mov_b32_e32 v11, v143
	v_cvt_pk_fp8_f32 v11, v12, v15
	v_mul_f32_e32 v13, 0x43000000, v114
	v_cvt_pk_fp8_f32 v10, v13, v14 op_sel:[0,0,1]
	v_mul_f32_e32 v12, 0x43000000, v130
	v_mul_f32_e32 v13, 0x43000000, v134
	v_cvt_pk_fp8_f32 v11, v12, v13 op_sel:[0,0,1]
	v_mul_f32_e32 v13, 0x43000000, v71
	v_mul_f32_e32 v14, 0x43000000, v75
	v_mov_b32_e32 v12, v143
	v_cvt_pk_fp8_f32 v12, v13, v14
	v_mul_f32_e32 v14, 0x43000000, v87
	v_mov_b32_e32 v13, v143
	v_cvt_pk_fp8_f32 v13, v14, v17
	v_mul_f32_e32 v15, 0x43000000, v79
	v_cvt_pk_fp8_f32 v12, v15, v16 op_sel:[0,0,1]
	v_mul_f32_e32 v14, 0x43000000, v95
	v_mul_f32_e32 v15, 0x43000000, v103
	v_cvt_pk_fp8_f32 v13, v14, v15 op_sel:[0,0,1]
	v_mul_f32_e32 v15, 0x43000000, v107
	v_mul_f32_e32 v16, 0x43000000, v111
	v_mov_b32_e32 v14, v143
	v_cvt_pk_fp8_f32 v14, v15, v16
	v_mul_f32_e32 v16, 0x43000000, v123
	v_mov_b32_e32 v15, v143
	v_cvt_pk_fp8_f32 v15, v16, v19
	v_mul_f32_e32 v17, 0x43000000, v115
	v_cvt_pk_fp8_f32 v14, v17, v18 op_sel:[0,0,1]
	v_mul_f32_e32 v16, 0x43000000, v131
	v_mul_f32_e32 v17, 0x43000000, v135
	v_cvt_pk_fp8_f32 v15, v16, v17 op_sel:[0,0,1]
	ds_write_b128 v194, v[0:3] offset:32
	ds_write_b128 v194, v[4:7] offset:2592
	ds_write_b128 v194, v[8:11] offset:5152
	ds_write_b128 v194, v[12:15] offset:7712
	s_waitcnt lgkmcnt(0)
	ds_read_b128 v[0:3], v195
	v_add_u32_e32 v4, s6, v181
	v_ashrrev_i32_e32 v5, 31, v4
	v_lshl_add_u64 v[8:9], s[68:69], 0, v[144:145]
	v_lshlrev_b64 v[4:5], 10, v[4:5]
	v_lshl_add_u64 v[10:11], v[8:9], 0, v[4:5]
	ds_read_b128 v[4:7], v195 offset:1280
	s_waitcnt lgkmcnt(1)
	global_store_dwordx4 v[10:11], v[0:3], off nt
	s_nop 1
	v_add_u32_e32 v0, s6, v182
	v_ashrrev_i32_e32 v1, 31, v0
	v_lshlrev_b64 v[0:1], 10, v[0:1]
	v_lshl_add_u64 v[0:1], v[8:9], 0, v[0:1]
	s_waitcnt lgkmcnt(0)
	global_store_dwordx4 v[0:1], v[4:7], off nt
	ds_read_b128 v[0:3], v195 offset:2560
	s_nop 0
	v_add_u32_e32 v4, s6, v183
	v_ashrrev_i32_e32 v5, 31, v4
	v_lshlrev_b64 v[4:5], 10, v[4:5]
	v_lshl_add_u64 v[10:11], v[8:9], 0, v[4:5]
	ds_read_b128 v[4:7], v195 offset:3840
	s_waitcnt lgkmcnt(1)
	global_store_dwordx4 v[10:11], v[0:3], off nt
	s_nop 1
	v_add_u32_e32 v0, s6, v184
	v_ashrrev_i32_e32 v1, 31, v0
	v_lshlrev_b64 v[0:1], 10, v[0:1]
	v_lshl_add_u64 v[0:1], v[8:9], 0, v[0:1]
	s_waitcnt lgkmcnt(0)
	global_store_dwordx4 v[0:1], v[4:7], off nt
	ds_read_b128 v[0:3], v195 offset:5120
	s_nop 0
	v_add_u32_e32 v4, s6, v185
	v_ashrrev_i32_e32 v5, 31, v4
	v_lshlrev_b64 v[4:5], 10, v[4:5]
	v_lshl_add_u64 v[10:11], v[8:9], 0, v[4:5]
	ds_read_b128 v[4:7], v195 offset:6400
	s_waitcnt lgkmcnt(1)
	global_store_dwordx4 v[10:11], v[0:3], off nt
	s_nop 1
	v_add_u32_e32 v0, s6, v186
	v_ashrrev_i32_e32 v1, 31, v0
	v_lshlrev_b64 v[0:1], 10, v[0:1]
	v_lshl_add_u64 v[0:1], v[8:9], 0, v[0:1]
	s_waitcnt lgkmcnt(0)
	global_store_dwordx4 v[0:1], v[4:7], off nt
	ds_read_b128 v[0:3], v195 offset:7680
	s_nop 0
	v_add_u32_e32 v4, s6, v187
	v_ashrrev_i32_e32 v5, 31, v4
	v_lshlrev_b64 v[4:5], 10, v[4:5]
	v_lshl_add_u64 v[10:11], v[8:9], 0, v[4:5]
	ds_read_b128 v[4:7], v195 offset:8960
	s_waitcnt lgkmcnt(1)
	global_store_dwordx4 v[10:11], v[0:3], off nt
	s_nop 1
	v_add_u32_e32 v0, s6, v188
	v_ashrrev_i32_e32 v1, 31, v0
	v_lshlrev_b64 v[0:1], 10, v[0:1]
	v_lshl_add_u64 v[0:1], v[8:9], 0, v[0:1]
	s_waitcnt lgkmcnt(0)
	global_store_dwordx4 v[0:1], v[4:7], off nt
	s_waitcnt lgkmcnt(0)

; #define LAS __attribute__((address_space(3)))
; template <int QPERM>
; __device__ __forceinline__ void transpose_item(const float* W, int K, int N, bf16_t* WT, LAS float* scr, int item, int lane) {
;     const int nblk = N / 32, kb = item / nblk, nb = item % nblk, k0 = 64 * kb, n0 = 32 * nb;
; #pragma unroll 8
;     for (int i = 0; i < 32; ++i) { const int kk = 2 * i + (lane >> 5); scr[kk * 33 + (lane & 31)] = W[(size_t)(k0 + kk) * N + n0 + (lane & 31)]; }
.LBB0_49:
	s_lshl_b32 s67, s4, 1
	s_lshl_b32 s68, s8, 1
	v_add_u32_e32 v20, s67, v2
	v_add_u32_e32 v18, s68, v3
	v_add_u32_e32 v22, s68, v5
	v_add_u32_e32 v24, s67, v4
	v_add_u32_e32 v26, s68, v7
	v_add_u32_e32 v28, s67, v6
	v_add_u32_e32 v30, s68, v9
	v_add_u32_e32 v32, s67, v8
	v_add_u32_e32 v34, s68, v11
	v_add_u32_e32 v36, s67, v10
	v_add_u32_e32 v38, s68, v13
	v_add_u32_e32 v40, s67, v12
	v_add_u32_e32 v42, s68, v15
	v_add_u32_e32 v44, s67, v14
	v_add_u32_e32 v46, s68, v17
	v_add_u32_e32 v48, s67, v16
	v_ashrrev_i32_e32 v21, 31, v20
	v_ashrrev_i32_e32 v19, 31, v18
	v_ashrrev_i32_e32 v25, 31, v24
	v_ashrrev_i32_e32 v23, 31, v22
	v_ashrrev_i32_e32 v29, 31, v28
	v_ashrrev_i32_e32 v27, 31, v26
	v_ashrrev_i32_e32 v33, 31, v32
	v_ashrrev_i32_e32 v31, 31, v30
	v_ashrrev_i32_e32 v37, 31, v36
	v_ashrrev_i32_e32 v35, 31, v34
	v_ashrrev_i32_e32 v41, 31, v40
	v_ashrrev_i32_e32 v39, 31, v38
	v_ashrrev_i32_e32 v45, 31, v44
	v_ashrrev_i32_e32 v43, 31, v42
	v_ashrrev_i32_e32 v49, 31, v48
	v_ashrrev_i32_e32 v47, 31, v46
	v_lshlrev_b64 v[20:21], 12, v[20:21]
	v_lshlrev_b64 v[18:19], 12, v[18:19]
	v_lshlrev_b64 v[22:23], 12, v[22:23]
	v_lshlrev_b64 v[24:25], 12, v[24:25]
	v_lshlrev_b64 v[26:27], 12, v[26:27]
	v_lshlrev_b64 v[28:29], 12, v[28:29]
	v_lshlrev_b64 v[30:31], 12, v[30:31]
	v_lshlrev_b64 v[32:33], 12, v[32:33]
	v_lshlrev_b64 v[34:35], 12, v[34:35]
	v_lshlrev_b64 v[36:37], 12, v[36:37]
	v_lshlrev_b64 v[38:39], 12, v[38:39]
	v_lshlrev_b64 v[40:41], 12, v[40:41]
	v_lshlrev_b64 v[42:43], 12, v[42:43]
	v_lshlrev_b64 v[44:45], 12, v[44:45]
	v_lshlrev_b64 v[46:47], 12, v[46:47]
	v_lshlrev_b64 v[48:49], 12, v[48:49]
	v_lshl_add_u64 v[20:21], v[0:1], 0, v[20:21]
	v_lshl_add_u64 v[18:19], v[0:1], 0, v[18:19]
	v_lshl_add_u64 v[24:25], v[0:1], 0, v[24:25]
	v_lshl_add_u64 v[22:23], v[0:1], 0, v[22:23]
	v_lshl_add_u64 v[28:29], v[0:1], 0, v[28:29]
	v_lshl_add_u64 v[26:27], v[0:1], 0, v[26:27]
	v_lshl_add_u64 v[32:33], v[0:1], 0, v[32:33]
	v_lshl_add_u64 v[30:31], v[0:1], 0, v[30:31]
	v_lshl_add_u64 v[36:37], v[0:1], 0, v[36:37]
	v_lshl_add_u64 v[34:35], v[0:1], 0, v[34:35]
	v_lshl_add_u64 v[40:41], v[0:1], 0, v[40:41]
	v_lshl_add_u64 v[38:39], v[0:1], 0, v[38:39]
	v_lshl_add_u64 v[44:45], v[0:1], 0, v[44:45]
	v_lshl_add_u64 v[42:43], v[0:1], 0, v[42:43]
	v_lshl_add_u64 v[48:49], v[0:1], 0, v[48:49]
	v_lshl_add_u64 v[46:47], v[0:1], 0, v[46:47]
	global_load_dword v50, v[20:21], off nt
	global_load_dword v51, v[18:19], off nt
	global_load_dword v52, v[24:25], off nt
	global_load_dword v53, v[22:23], off nt
	global_load_dword v54, v[28:29], off nt
	global_load_dword v55, v[26:27], off nt
	global_load_dword v56, v[32:33], off nt
	global_load_dword v57, v[30:31], off nt
	global_load_dword v58, v[36:37], off nt
	global_load_dword v59, v[34:35], off nt
	global_load_dword v60, v[40:41], off nt
	global_load_dword v61, v[38:39], off nt
	global_load_dword v62, v[44:45], off nt
	global_load_dword v63, v[42:43], off nt
	global_load_dword v64, v[48:49], off nt
	global_load_dword v65, v[46:47], off nt
	s_add_i32 s4, s4, 16
	s_add_i32 s8, s8, 16
	s_add_i32 s9, s9, -16
	v_add_u32_e32 v18, s67, v146
	v_add_u32_e32 v20, s68, v141
	v_add_u32_e32 v24, s68, v147
	v_add_u32_e32 v22, s67, v166
	v_add_u32_e32 v28, s68, v151
	v_add_u32_e32 v26, s67, v168
	v_add_u32_e32 v32, s68, v167
	v_add_u32_e32 v30, s67, v170
	v_add_u32_e32 v36, s68, v169
	v_add_u32_e32 v34, s67, v172
	v_add_u32_e32 v40, s68, v171
	v_add_u32_e32 v38, s67, v174
	v_add_u32_e32 v44, s68, v173
	v_add_u32_e32 v42, s67, v176
	v_add_u32_e32 v48, s68, v175
	v_add_u32_e32 v46, s67, v178
	s_cmp_lg_u32 s9, 0
	v_mad_u64_u32 v[18:19], s[68:69], v18, s13, v[150:151]
	v_mad_u64_u32 v[20:21], s[68:69], v20, s13, v[150:151]
	v_mad_u64_u32 v[22:23], s[68:69], v22, s13, v[150:151]
	v_mad_u64_u32 v[24:25], s[68:69], v24, s13, v[150:151]
	v_mad_u64_u32 v[26:27], s[68:69], v26, s13, v[150:151]
	v_mad_u64_u32 v[28:29], s[68:69], v28, s13, v[150:151]
	v_mad_u64_u32 v[30:31], s[68:69], v30, s13, v[150:151]
	v_mad_u64_u32 v[32:33], s[68:69], v32, s13, v[150:151]
	v_mad_u64_u32 v[34:35], s[68:69], v34, s13, v[150:151]
	v_mad_u64_u32 v[36:37], s[68:69], v36, s13, v[150:151]
	v_mad_u64_u32 v[38:39], s[68:69], v38, s13, v[150:151]
	v_mad_u64_u32 v[40:41], s[68:69], v40, s13, v[150:151]
	v_mad_u64_u32 v[42:43], s[68:69], v42, s13, v[150:151]
	v_mad_u64_u32 v[44:45], s[68:69], v44, s13, v[150:151]
	v_mad_u64_u32 v[46:47], s[68:69], v46, s13, v[150:151]
	v_mad_u64_u32 v[48:49], s[68:69], v48, s13, v[150:151]
	s_waitcnt vmcnt(15)
	ds_write_b32 v18, v50
	s_waitcnt vmcnt(14)
	ds_write_b32 v20, v51
	s_waitcnt vmcnt(13)
	ds_write_b32 v22, v52
	s_waitcnt vmcnt(12)
	ds_write_b32 v24, v53
	s_waitcnt vmcnt(11)
	ds_write_b32 v26, v54
	s_waitcnt vmcnt(10)
	ds_write_b32 v28, v55
	s_waitcnt vmcnt(9)
	ds_write_b32 v30, v56
	s_waitcnt vmcnt(8)
	ds_write_b32 v32, v57
	s_waitcnt vmcnt(7)
	ds_write_b32 v34, v58
	s_waitcnt vmcnt(6)
	ds_write_b32 v36, v59
	s_waitcnt vmcnt(5)
	ds_write_b32 v38, v60
	s_waitcnt vmcnt(4)
	ds_write_b32 v40, v61
	s_waitcnt vmcnt(3)
	ds_write_b32 v42, v62
	s_waitcnt vmcnt(2)
	ds_write_b32 v44, v63
	s_waitcnt vmcnt(1)
	ds_write_b32 v46, v64
	s_waitcnt vmcnt(0)
	ds_write_b32 v48, v65
	s_cbranch_scc1 .LBB0_49
; #define LAS __attribute__((address_space(3)))
; __device__ __forceinline__ unsigned pk2(float lo, float hi) { unsigned r; asm("v_cvt_pk_bf16_f32 %0, %1, %2" : "=v"(r) : "v"(lo), "v"(hi)); return r; }
; template <int QPERM>
; __device__ __forceinline__ void transpose_item(const float* W, int K, int N, bf16_t* WT, LAS float* scr, int item, int lane) {
;     ...
;     asm volatile("s_waitcnt lgkmcnt(0)" ::: "memory");
;     const int c = lane & 7;
; #pragma unroll
;     for (int j = 0; j < 4; ++j) { const int n = (lane >> 3) + 8 * j; const LAS float* s = scr + (8 * c) * 33 + n;
;         u32x4 o; o.x = pk2(s[0 * 33], s[1 * 33]); o.y = pk2(s[2 * 33], s[3 * 33]); o.z = pk2(s[4 * 33], s[5 * 33]); o.w = pk2(s[6 * 33], s[7 * 33]);
;         int dn = n0 + n;
;         if (QPERM == 1) { const int h = dn / 192, d = dn % 192; if (d >= 128) { const int jj = d - 128, a = jj >> 5, p = (jj >> 4) & 1, f = jj & 15; dn = h * 192 + 128 + 2 * (a * 16 + f) + p; } }
;         if (QPERM == 2) { const int h = dn >> 8, j = dn & 255; dn = (j < 128) ? h * 128 + j : 512 + h * 128 + (j - 128); }
;         *(u32x4*)(WT + (size_t)dn * K + k0 + 8 * c) = o; }
;     asm volatile("s_waitcnt lgkmcnt(0)" ::: "memory");
	s_waitcnt lgkmcnt(0)
	ds_read2_b32 v[4:5], v190 offset0:33 offset1:41
	ds_read2_b32 v[6:7], v190 offset1:8
	ds_read2_b32 v[8:9], v190 offset0:66 offset1:74
	ds_read2_b32 v[10:11], v190 offset0:99 offset1:107
	ds_read2_b32 v[12:13], v190 offset0:132 offset1:140
	ds_read2_b32 v[14:15], v190 offset0:165 offset1:173
	ds_read2_b32 v[16:17], v190 offset0:198 offset1:206
	ds_read2_b32 v[18:19], v190 offset0:231 offset1:239
	v_add_u32_e32 v22, s6, v189
	s_lshl_b32 s4, s7, 1
	v_ashrrev_i32_e32 v23, 31, v22
	v_lshl_add_u64 v[20:21], v[152:153], 0, s[4:5]
	v_lshlrev_b64 v[22:23], 11, v[22:23]
	s_waitcnt lgkmcnt(6)
	v_cvt_pk_bf16_f32 v0, v6, v4
	v_lshl_add_u64 v[22:23], v[20:21], 0, v[22:23]
	v_add_u32_e32 v4, s6, v191
	s_waitcnt lgkmcnt(4)
	v_cvt_pk_bf16_f32 v1, v8, v10
	s_waitcnt lgkmcnt(2)
	v_cvt_pk_bf16_f32 v2, v12, v14
	s_waitcnt lgkmcnt(0)
	v_cvt_pk_bf16_f32 v3, v16, v18
	global_store_dwordx4 v[22:23], v[0:3], off nt
	s_nop 1
	v_cvt_pk_bf16_f32 v0, v7, v5
	v_ashrrev_i32_e32 v5, 31, v4
	v_lshlrev_b64 v[4:5], 11, v[4:5]
	v_cvt_pk_bf16_f32 v1, v9, v11
	v_cvt_pk_bf16_f32 v2, v13, v15
	v_cvt_pk_bf16_f32 v3, v17, v19
	v_lshl_add_u64 v[4:5], v[20:21], 0, v[4:5]
	ds_read2_b32 v[6:7], v190 offset0:16 offset1:24
	ds_read2_b32 v[8:9], v190 offset0:49 offset1:57
	ds_read2_b32 v[10:11], v190 offset0:82 offset1:90
	ds_read2_b32 v[12:13], v190 offset0:115 offset1:123
	ds_read2_b32 v[14:15], v190 offset0:148 offset1:156
	ds_read2_b32 v[16:17], v190 offset0:181 offset1:189
	ds_read2_b32 v[18:19], v190 offset0:214 offset1:222
	ds_read2_b32 v[22:23], v190 offset0:247 offset1:255
	global_store_dwordx4 v[4:5], v[0:3], off nt
	v_add_u32_e32 v4, s6, v192
	v_ashrrev_i32_e32 v5, 31, v4
	v_lshlrev_b64 v[4:5], 11, v[4:5]
	v_lshl_add_u64 v[4:5], v[20:21], 0, v[4:5]
	s_waitcnt lgkmcnt(6)
	v_cvt_pk_bf16_f32 v0, v6, v8
	s_waitcnt lgkmcnt(4)
	v_cvt_pk_bf16_f32 v1, v10, v12
	s_waitcnt lgkmcnt(2)
	v_cvt_pk_bf16_f32 v2, v14, v16
	s_waitcnt lgkmcnt(0)
	v_cvt_pk_bf16_f32 v3, v18, v22
	global_store_dwordx4 v[4:5], v[0:3], off nt
	v_add_u32_e32 v4, s6, v193
	v_ashrrev_i32_e32 v5, 31, v4
	v_lshlrev_b64 v[4:5], 11, v[4:5]
	v_lshl_add_u64 v[4:5], v[20:21], 0, v[4:5]
	v_cvt_pk_bf16_f32 v0, v7, v9
	v_cvt_pk_bf16_f32 v1, v11, v13
	v_cvt_pk_bf16_f32 v2, v15, v17
	v_cvt_pk_bf16_f32 v3, v19, v23
	global_store_dwordx4 v[4:5], v[0:3], off nt
	s_waitcnt lgkmcnt(0)

; #define LAS __attribute__((address_space(3)))
; template <int QPERM>
; __device__ __forceinline__ void transpose_item(const float* W, int K, int N, bf16_t* WT, LAS float* scr, int item, int lane) {
;     const int nblk = N / 32, kb = item / nblk, nb = item % nblk, k0 = 64 * kb, n0 = 32 * nb;
; #pragma unroll 8
;     for (int i = 0; i < 32; ++i) { const int kk = 2 * i + (lane >> 5); scr[kk * 33 + (lane & 31)] = W[(size_t)(k0 + kk) * N + n0 + (lane & 31)]; }
.LBB0_54:
	s_lshl_b32 s67, s4, 1
	s_lshl_b32 s68, s8, 1
	v_add_u32_e32 v20, s67, v2
	v_add_u32_e32 v18, s68, v3
	v_add_u32_e32 v22, s68, v5
	v_add_u32_e32 v24, s67, v4
	v_add_u32_e32 v26, s68, v7
	v_add_u32_e32 v28, s67, v6
	v_add_u32_e32 v30, s68, v9
	v_add_u32_e32 v32, s67, v8
	v_add_u32_e32 v34, s68, v11
	v_add_u32_e32 v36, s67, v10
	v_add_u32_e32 v38, s68, v13
	v_add_u32_e32 v40, s67, v12
	v_add_u32_e32 v42, s68, v15
	v_add_u32_e32 v44, s67, v14
	v_add_u32_e32 v46, s68, v17
	v_add_u32_e32 v48, s67, v16
	v_ashrrev_i32_e32 v21, 31, v20
	v_ashrrev_i32_e32 v19, 31, v18
	v_ashrrev_i32_e32 v25, 31, v24
	v_ashrrev_i32_e32 v23, 31, v22
	v_ashrrev_i32_e32 v29, 31, v28
	v_ashrrev_i32_e32 v27, 31, v26
	v_ashrrev_i32_e32 v33, 31, v32
	v_ashrrev_i32_e32 v31, 31, v30
	v_ashrrev_i32_e32 v37, 31, v36
	v_ashrrev_i32_e32 v35, 31, v34
	v_ashrrev_i32_e32 v41, 31, v40
	v_ashrrev_i32_e32 v39, 31, v38
	v_ashrrev_i32_e32 v45, 31, v44
	v_ashrrev_i32_e32 v43, 31, v42
	v_ashrrev_i32_e32 v49, 31, v48
	v_ashrrev_i32_e32 v47, 31, v46
	v_lshlrev_b64 v[20:21], 12, v[20:21]
	v_lshlrev_b64 v[18:19], 12, v[18:19]
	v_lshlrev_b64 v[22:23], 12, v[22:23]
	v_lshlrev_b64 v[24:25], 12, v[24:25]
	v_lshlrev_b64 v[26:27], 12, v[26:27]
	v_lshlrev_b64 v[28:29], 12, v[28:29]
	v_lshlrev_b64 v[30:31], 12, v[30:31]
	v_lshlrev_b64 v[32:33], 12, v[32:33]
	v_lshlrev_b64 v[34:35], 12, v[34:35]
	v_lshlrev_b64 v[36:37], 12, v[36:37]
	v_lshlrev_b64 v[38:39], 12, v[38:39]
	v_lshlrev_b64 v[40:41], 12, v[40:41]
	v_lshlrev_b64 v[42:43], 12, v[42:43]
	v_lshlrev_b64 v[44:45], 12, v[44:45]
	v_lshlrev_b64 v[46:47], 12, v[46:47]
	v_lshlrev_b64 v[48:49], 12, v[48:49]
	v_lshl_add_u64 v[20:21], v[0:1], 0, v[20:21]
	v_lshl_add_u64 v[18:19], v[0:1], 0, v[18:19]
	v_lshl_add_u64 v[24:25], v[0:1], 0, v[24:25]
	v_lshl_add_u64 v[22:23], v[0:1], 0, v[22:23]
	v_lshl_add_u64 v[28:29], v[0:1], 0, v[28:29]
	v_lshl_add_u64 v[26:27], v[0:1], 0, v[26:27]
	v_lshl_add_u64 v[32:33], v[0:1], 0, v[32:33]
	v_lshl_add_u64 v[30:31], v[0:1], 0, v[30:31]
	v_lshl_add_u64 v[36:37], v[0:1], 0, v[36:37]
	v_lshl_add_u64 v[34:35], v[0:1], 0, v[34:35]
	v_lshl_add_u64 v[40:41], v[0:1], 0, v[40:41]
	v_lshl_add_u64 v[38:39], v[0:1], 0, v[38:39]
	v_lshl_add_u64 v[44:45], v[0:1], 0, v[44:45]
	v_lshl_add_u64 v[42:43], v[0:1], 0, v[42:43]
	v_lshl_add_u64 v[48:49], v[0:1], 0, v[48:49]
	v_lshl_add_u64 v[46:47], v[0:1], 0, v[46:47]
	global_load_dword v50, v[20:21], off nt
	global_load_dword v51, v[18:19], off nt
	global_load_dword v52, v[24:25], off nt
	global_load_dword v53, v[22:23], off nt
	global_load_dword v54, v[28:29], off nt
	global_load_dword v55, v[26:27], off nt
	global_load_dword v56, v[32:33], off nt
	global_load_dword v57, v[30:31], off nt
	global_load_dword v58, v[36:37], off nt
	global_load_dword v59, v[34:35], off nt
	global_load_dword v60, v[40:41], off nt
	global_load_dword v61, v[38:39], off nt
	global_load_dword v62, v[44:45], off nt
	global_load_dword v63, v[42:43], off nt
	global_load_dword v64, v[48:49], off nt
	global_load_dword v65, v[46:47], off nt
	s_add_i32 s4, s4, 16
	s_add_i32 s8, s8, 16
	s_add_i32 s9, s9, -16
	v_add_u32_e32 v18, s67, v146
	v_add_u32_e32 v20, s68, v141
	v_add_u32_e32 v24, s68, v147
	v_add_u32_e32 v22, s67, v166
	v_add_u32_e32 v28, s68, v151
	v_add_u32_e32 v26, s67, v168
	v_add_u32_e32 v32, s68, v167
	v_add_u32_e32 v30, s67, v170
	v_add_u32_e32 v36, s68, v169
	v_add_u32_e32 v34, s67, v172
	v_add_u32_e32 v40, s68, v171
	v_add_u32_e32 v38, s67, v174
	v_add_u32_e32 v44, s68, v173
	v_add_u32_e32 v42, s67, v176
	v_add_u32_e32 v48, s68, v175
	v_add_u32_e32 v46, s67, v178
	s_cmp_lg_u32 s9, 0
	v_mad_u64_u32 v[18:19], s[68:69], v18, s13, v[150:151]
	v_mad_u64_u32 v[20:21], s[68:69], v20, s13, v[150:151]
	v_mad_u64_u32 v[22:23], s[68:69], v22, s13, v[150:151]
	v_mad_u64_u32 v[24:25], s[68:69], v24, s13, v[150:151]
	v_mad_u64_u32 v[26:27], s[68:69], v26, s13, v[150:151]
	v_mad_u64_u32 v[28:29], s[68:69], v28, s13, v[150:151]
	v_mad_u64_u32 v[30:31], s[68:69], v30, s13, v[150:151]
	v_mad_u64_u32 v[32:33], s[68:69], v32, s13, v[150:151]
	v_mad_u64_u32 v[34:35], s[68:69], v34, s13, v[150:151]
	v_mad_u64_u32 v[36:37], s[68:69], v36, s13, v[150:151]
	v_mad_u64_u32 v[38:39], s[68:69], v38, s13, v[150:151]
	v_mad_u64_u32 v[40:41], s[68:69], v40, s13, v[150:151]
	v_mad_u64_u32 v[42:43], s[68:69], v42, s13, v[150:151]
	v_mad_u64_u32 v[44:45], s[68:69], v44, s13, v[150:151]
	v_mad_u64_u32 v[46:47], s[68:69], v46, s13, v[150:151]
	v_mad_u64_u32 v[48:49], s[68:69], v48, s13, v[150:151]
	s_waitcnt vmcnt(15)
	ds_write_b32 v18, v50
	s_waitcnt vmcnt(14)
	ds_write_b32 v20, v51
	s_waitcnt vmcnt(13)
	ds_write_b32 v22, v52
	s_waitcnt vmcnt(12)
	ds_write_b32 v24, v53
	s_waitcnt vmcnt(11)
	ds_write_b32 v26, v54
	s_waitcnt vmcnt(10)
	ds_write_b32 v28, v55
	s_waitcnt vmcnt(9)
	ds_write_b32 v30, v56
	s_waitcnt vmcnt(8)
	ds_write_b32 v32, v57
	s_waitcnt vmcnt(7)
	ds_write_b32 v34, v58
	s_waitcnt vmcnt(6)
	ds_write_b32 v36, v59
	s_waitcnt vmcnt(5)
	ds_write_b32 v38, v60
	s_waitcnt vmcnt(4)
	ds_write_b32 v40, v61
	s_waitcnt vmcnt(3)
	ds_write_b32 v42, v62
	s_waitcnt vmcnt(2)
	ds_write_b32 v44, v63
	s_waitcnt vmcnt(1)
	ds_write_b32 v46, v64
	s_waitcnt vmcnt(0)
	ds_write_b32 v48, v65
	s_cbranch_scc1 .LBB0_54
; #define LAS __attribute__((address_space(3)))
; __device__ __forceinline__ unsigned pk2(float lo, float hi) { unsigned r; asm("v_cvt_pk_bf16_f32 %0, %1, %2" : "=v"(r) : "v"(lo), "v"(hi)); return r; }
; template <int QPERM>
; __device__ __forceinline__ void transpose_item(const float* W, int K, int N, bf16_t* WT, LAS float* scr, int item, int lane) {
;     ...
;     asm volatile("s_waitcnt lgkmcnt(0)" ::: "memory");
;     const int c = lane & 7;
; #pragma unroll
;     for (int j = 0; j < 4; ++j) { const int n = (lane >> 3) + 8 * j; const LAS float* s = scr + (8 * c) * 33 + n;
;         u32x4 o; o.x = pk2(s[0 * 33], s[1 * 33]); o.y = pk2(s[2 * 33], s[3 * 33]); o.z = pk2(s[4 * 33], s[5 * 33]); o.w = pk2(s[6 * 33], s[7 * 33]);
;         int dn = n0 + n;
;         if (QPERM == 1) { const int h = dn / 192, d = dn % 192; if (d >= 128) { const int jj = d - 128, a = jj >> 5, p = (jj >> 4) & 1, f = jj & 15; dn = h * 192 + 128 + 2 * (a * 16 + f) + p; } }
;         if (QPERM == 2) { const int h = dn >> 8, j = dn & 255; dn = (j < 128) ? h * 128 + j : 512 + h * 128 + (j - 128); }
;         *(u32x4*)(WT + (size_t)dn * K + k0 + 8 * c) = o; }
;     asm volatile("s_waitcnt lgkmcnt(0)" ::: "memory");
	s_waitcnt lgkmcnt(0)
	ds_read2_b32 v[4:5], v190 offset0:33 offset1:41
	ds_read2_b32 v[6:7], v190 offset1:8
	ds_read2_b32 v[8:9], v190 offset0:66 offset1:74
	ds_read2_b32 v[10:11], v190 offset0:99 offset1:107
	ds_read2_b32 v[12:13], v190 offset0:132 offset1:140
	ds_read2_b32 v[14:15], v190 offset0:165 offset1:173
	ds_read2_b32 v[16:17], v190 offset0:198 offset1:206
	ds_read2_b32 v[18:19], v190 offset0:231 offset1:239
	s_waitcnt lgkmcnt(6)
	v_cvt_pk_bf16_f32 v0, v6, v4
	v_add_u32_e32 v4, s6, v189
	v_and_b32_e32 v6, 0xff, v4
	v_ashrrev_i32_e32 v4, 1, v4
	v_and_b32_e32 v4, 0xffffff80, v4
	s_waitcnt lgkmcnt(4)
	v_cvt_pk_bf16_f32 v1, v8, v10
	v_or_b32_e32 v8, v4, v6
	v_add3_u32 v4, v6, v4, s60
	v_cmp_gt_u32_e32 vcc, s59, v6
	s_lshl_b32 s4, s7, 1
	v_lshl_add_u64 v[20:21], v[156:157], 0, s[4:5]
	v_cndmask_b32_e32 v22, v4, v8, vcc
	v_ashrrev_i32_e32 v23, 31, v22
	v_lshlrev_b64 v[22:23], 9, v[22:23]
	v_lshl_add_u64 v[22:23], v[20:21], 0, v[22:23]
	v_add_u32_e32 v4, s6, v191
	s_waitcnt lgkmcnt(2)
	v_cvt_pk_bf16_f32 v2, v12, v14
	s_waitcnt lgkmcnt(0)
	v_cvt_pk_bf16_f32 v3, v16, v18
	global_store_dwordx4 v[22:23], v[0:3], off nt
	s_nop 1
	v_cvt_pk_bf16_f32 v0, v7, v5
	v_and_b32_e32 v5, 0xff, v4
	v_ashrrev_i32_e32 v4, 1, v4
	v_and_b32_e32 v4, 0xffffff80, v4
	v_or_b32_e32 v6, v4, v5
	v_add3_u32 v4, v5, v4, s60
	v_cmp_gt_u32_e32 vcc, s59, v5
	v_cvt_pk_bf16_f32 v1, v9, v11
	v_cvt_pk_bf16_f32 v2, v13, v15
	v_cvt_pk_bf16_f32 v3, v17, v19
	s_nop 1
	v_cndmask_b32_e32 v4, v4, v6, vcc
	v_ashrrev_i32_e32 v5, 31, v4
	v_lshlrev_b64 v[4:5], 9, v[4:5]
	v_lshl_add_u64 v[4:5], v[20:21], 0, v[4:5]
	ds_read2_b32 v[6:7], v190 offset0:16 offset1:24
	ds_read2_b32 v[8:9], v190 offset0:49 offset1:57
	ds_read2_b32 v[10:11], v190 offset0:82 offset1:90
	ds_read2_b32 v[12:13], v190 offset0:115 offset1:123
	ds_read2_b32 v[14:15], v190 offset0:148 offset1:156
	ds_read2_b32 v[16:17], v190 offset0:181 offset1:189
	ds_read2_b32 v[18:19], v190 offset0:214 offset1:222
	ds_read2_b32 v[22:23], v190 offset0:247 offset1:255
	global_store_dwordx4 v[4:5], v[0:3], off nt
	v_add_u32_e32 v4, s6, v192
	v_and_b32_e32 v5, 0xff, v4
	v_ashrrev_i32_e32 v4, 1, v4
	v_and_b32_e32 v4, 0xffffff80, v4
	s_waitcnt lgkmcnt(6)
	v_cvt_pk_bf16_f32 v0, v6, v8
	v_or_b32_e32 v6, v4, v5
	v_add3_u32 v4, v5, v4, s60
	v_cmp_gt_u32_e32 vcc, s59, v5
	s_waitcnt lgkmcnt(4)
	v_cvt_pk_bf16_f32 v1, v10, v12
	s_waitcnt lgkmcnt(2)
	v_cvt_pk_bf16_f32 v2, v14, v16
	s_waitcnt lgkmcnt(0)
	v_cvt_pk_bf16_f32 v3, v18, v22
	v_cndmask_b32_e32 v4, v4, v6, vcc
	v_ashrrev_i32_e32 v5, 31, v4
	v_lshlrev_b64 v[4:5], 9, v[4:5]
	v_lshl_add_u64 v[4:5], v[20:21], 0, v[4:5]
	global_store_dwordx4 v[4:5], v[0:3], off nt
	v_add_u32_e32 v4, s6, v193
	v_and_b32_e32 v5, 0xff, v4
	v_ashrrev_i32_e32 v4, 1, v4
	v_and_b32_e32 v4, 0xffffff80, v4
	v_or_b32_e32 v6, v4, v5
	v_add3_u32 v4, v5, v4, s60
	v_cmp_gt_u32_e32 vcc, s59, v5
	v_cvt_pk_bf16_f32 v0, v7, v9
	v_cvt_pk_bf16_f32 v1, v11, v13
	v_cvt_pk_bf16_f32 v2, v15, v17
	v_cvt_pk_bf16_f32 v3, v19, v23
	s_nop 1
	v_cndmask_b32_e32 v4, v4, v6, vcc
	v_ashrrev_i32_e32 v5, 31, v4
	v_lshlrev_b64 v[4:5], 9, v[4:5]
	v_lshl_add_u64 v[4:5], v[20:21], 0, v[4:5]
	global_store_dwordx4 v[4:5], v[0:3], off nt
	s_waitcnt lgkmcnt(0)

; #define LAS __attribute__((address_space(3)))
; template <int QPERM>
; __device__ __forceinline__ void transpose_item(const float* W, int K, int N, bf16_t* WT, LAS float* scr, int item, int lane) {
;     const int nblk = N / 32, kb = item / nblk, nb = item % nblk, k0 = 64 * kb, n0 = 32 * nb;
; #pragma unroll 8
;     for (int i = 0; i < 32; ++i) { const int kk = 2 * i + (lane >> 5); scr[kk * 33 + (lane & 31)] = W[(size_t)(k0 + kk) * N + n0 + (lane & 31)]; }
.LBB0_59:
	s_lshl_b32 s67, s7, 1
	s_lshl_b32 s70, s4, 1
	v_add_u32_e32 v18, s67, v2
	v_add_u32_e32 v20, s70, v3
	v_add_u32_e32 v24, s70, v5
	v_add_u32_e32 v22, s67, v4
	v_add_u32_e32 v28, s70, v7
	v_add_u32_e32 v26, s67, v6
	v_add_u32_e32 v32, s70, v9
	v_add_u32_e32 v30, s67, v8
	v_add_u32_e32 v36, s70, v11
	v_add_u32_e32 v34, s67, v10
	v_add_u32_e32 v40, s70, v13
	v_add_u32_e32 v38, s67, v12
	v_add_u32_e32 v44, s70, v15
	v_add_u32_e32 v42, s67, v14
	v_add_u32_e32 v48, s70, v17
	v_add_u32_e32 v46, s67, v16
	v_mad_i64_i32 v[18:19], s[68:69], v18, s61, v[0:1]
	v_mad_i64_i32 v[20:21], s[68:69], v20, s61, v[0:1]
	v_mad_i64_i32 v[22:23], s[68:69], v22, s61, v[0:1]
	v_mad_i64_i32 v[24:25], s[68:69], v24, s61, v[0:1]
	v_mad_i64_i32 v[26:27], s[68:69], v26, s61, v[0:1]
	v_mad_i64_i32 v[28:29], s[68:69], v28, s61, v[0:1]
	v_mad_i64_i32 v[30:31], s[68:69], v30, s61, v[0:1]
	v_mad_i64_i32 v[32:33], s[68:69], v32, s61, v[0:1]
	v_mad_i64_i32 v[34:35], s[68:69], v34, s61, v[0:1]
	v_mad_i64_i32 v[36:37], s[68:69], v36, s61, v[0:1]
	v_mad_i64_i32 v[38:39], s[68:69], v38, s61, v[0:1]
	v_mad_i64_i32 v[40:41], s[68:69], v40, s61, v[0:1]
	v_mad_i64_i32 v[42:43], s[68:69], v42, s61, v[0:1]
	v_mad_i64_i32 v[44:45], s[68:69], v44, s61, v[0:1]
	v_mad_i64_i32 v[46:47], s[68:69], v46, s61, v[0:1]
	v_mad_i64_i32 v[48:49], s[68:69], v48, s61, v[0:1]
	global_load_dword v50, v[18:19], off nt
	global_load_dword v51, v[20:21], off nt
	global_load_dword v52, v[22:23], off nt
	global_load_dword v53, v[24:25], off nt
	global_load_dword v54, v[26:27], off nt
	global_load_dword v55, v[28:29], off nt
	global_load_dword v56, v[30:31], off nt
	global_load_dword v57, v[32:33], off nt
	global_load_dword v58, v[34:35], off nt
	global_load_dword v59, v[36:37], off nt
	global_load_dword v60, v[38:39], off nt
	global_load_dword v61, v[40:41], off nt
	global_load_dword v62, v[42:43], off nt
	global_load_dword v63, v[44:45], off nt
	global_load_dword v64, v[46:47], off nt
	global_load_dword v65, v[48:49], off nt
	s_add_i32 s7, s7, 16
	s_add_i32 s4, s4, 16
	s_add_i32 s6, s6, -16
	v_add_u32_e32 v18, s67, v146
	v_add_u32_e32 v20, s70, v141
	v_add_u32_e32 v24, s70, v147
	v_add_u32_e32 v22, s67, v166
	v_add_u32_e32 v28, s70, v151
	v_add_u32_e32 v26, s67, v168
	v_add_u32_e32 v32, s70, v167
	v_add_u32_e32 v30, s67, v170
	v_add_u32_e32 v36, s70, v169
	v_add_u32_e32 v34, s67, v172
	v_add_u32_e32 v40, s70, v171
	v_add_u32_e32 v38, s67, v174
	v_add_u32_e32 v44, s70, v173
	v_add_u32_e32 v42, s67, v176
	v_add_u32_e32 v48, s70, v175
	v_add_u32_e32 v46, s67, v178
	s_cmp_lg_u32 s6, 0
	v_mad_u64_u32 v[18:19], s[68:69], v18, s13, v[150:151]
	v_mad_u64_u32 v[20:21], s[68:69], v20, s13, v[150:151]
	v_mad_u64_u32 v[22:23], s[68:69], v22, s13, v[150:151]
	v_mad_u64_u32 v[24:25], s[68:69], v24, s13, v[150:151]
	v_mad_u64_u32 v[26:27], s[68:69], v26, s13, v[150:151]
	v_mad_u64_u32 v[28:29], s[68:69], v28, s13, v[150:151]
	v_mad_u64_u32 v[30:31], s[68:69], v30, s13, v[150:151]
	v_mad_u64_u32 v[32:33], s[68:69], v32, s13, v[150:151]
	v_mad_u64_u32 v[34:35], s[68:69], v34, s13, v[150:151]
	v_mad_u64_u32 v[36:37], s[68:69], v36, s13, v[150:151]
	v_mad_u64_u32 v[38:39], s[68:69], v38, s13, v[150:151]
	v_mad_u64_u32 v[40:41], s[68:69], v40, s13, v[150:151]
	v_mad_u64_u32 v[42:43], s[68:69], v42, s13, v[150:151]
	v_mad_u64_u32 v[44:45], s[68:69], v44, s13, v[150:151]
	v_mad_u64_u32 v[46:47], s[68:69], v46, s13, v[150:151]
	v_mad_u64_u32 v[48:49], s[68:69], v48, s13, v[150:151]
	s_waitcnt vmcnt(15)
	ds_write_b32 v18, v50
	s_waitcnt vmcnt(14)
	ds_write_b32 v20, v51
	s_waitcnt vmcnt(13)
	ds_write_b32 v22, v52
	s_waitcnt vmcnt(12)
	ds_write_b32 v24, v53
	s_waitcnt vmcnt(11)
	ds_write_b32 v26, v54
	s_waitcnt vmcnt(10)
	ds_write_b32 v28, v55
	s_waitcnt vmcnt(9)
	ds_write_b32 v30, v56
	s_waitcnt vmcnt(8)
	ds_write_b32 v32, v57
	s_waitcnt vmcnt(7)
	ds_write_b32 v34, v58
	s_waitcnt vmcnt(6)
	ds_write_b32 v36, v59
	s_waitcnt vmcnt(5)
	ds_write_b32 v38, v60
	s_waitcnt vmcnt(4)
	ds_write_b32 v40, v61
	s_waitcnt vmcnt(3)
	ds_write_b32 v42, v62
	s_waitcnt vmcnt(2)
	ds_write_b32 v44, v63
	s_waitcnt vmcnt(1)
	ds_write_b32 v46, v64
	s_waitcnt vmcnt(0)
	ds_write_b32 v48, v65
	s_cbranch_scc1 .LBB0_59
; #define LAS __attribute__((address_space(3)))
; __device__ __forceinline__ unsigned pk2(float lo, float hi) { unsigned r; asm("v_cvt_pk_bf16_f32 %0, %1, %2" : "=v"(r) : "v"(lo), "v"(hi)); return r; }
; template <int QPERM>
; __device__ __forceinline__ void transpose_item(const float* W, int K, int N, bf16_t* WT, LAS float* scr, int item, int lane) {
;     ...
;     asm volatile("s_waitcnt lgkmcnt(0)" ::: "memory");
;     const int c = lane & 7;
; #pragma unroll
;     for (int j = 0; j < 4; ++j) { const int n = (lane >> 3) + 8 * j; const LAS float* s = scr + (8 * c) * 33 + n;
;         u32x4 o; o.x = pk2(s[0 * 33], s[1 * 33]); o.y = pk2(s[2 * 33], s[3 * 33]); o.z = pk2(s[4 * 33], s[5 * 33]); o.w = pk2(s[6 * 33], s[7 * 33]);
;         int dn = n0 + n;
;         if (QPERM == 1) { const int h = dn / 192, d = dn % 192; if (d >= 128) { const int jj = d - 128, a = jj >> 5, p = (jj >> 4) & 1, f = jj & 15; dn = h * 192 + 128 + 2 * (a * 16 + f) + p; } }
;         if (QPERM == 2) { const int h = dn >> 8, j = dn & 255; dn = (j < 128) ? h * 128 + j : 512 + h * 128 + (j - 128); }
;         *(u32x4*)(WT + (size_t)dn * K + k0 + 8 * c) = o; }
;     asm volatile("s_waitcnt lgkmcnt(0)" ::: "memory");
	s_waitcnt lgkmcnt(0)
	ds_read2_b32 v[0:1], v190 offset1:33
	ds_read2_b32 v[2:3], v190 offset0:66 offset1:99
	ds_read2_b32 v[4:5], v190 offset0:132 offset1:165
	ds_read2_b32 v[6:7], v190 offset0:198 offset1:231
	s_waitcnt lgkmcnt(3)
	v_cvt_pk_bf16_f32 v0, v0, v1
	s_waitcnt lgkmcnt(2)
	v_cvt_pk_bf16_f32 v1, v2, v3
	s_waitcnt lgkmcnt(1)
	v_cvt_pk_bf16_f32 v2, v4, v5
	s_waitcnt lgkmcnt(0)
	v_cvt_pk_bf16_f32 v3, v6, v7
	v_add_u32_e32 v6, s8, v189
	v_mul_hi_i32 v4, v6, s62
	v_lshrrev_b32_e32 v5, 31, v4
	v_lshrrev_b32_e32 v4, 5, v4
	v_add_u32_e32 v4, v4, v5
	v_mul_lo_u32 v4, v4, s58
	v_sub_u32_e32 v4, v6, v4
	v_cmp_lt_i32_e32 vcc, s63, v4
	s_and_saveexec_b64 s[6:7], vcc
	v_bfe_u32 v5, v4, 4, 1
	v_lshlrev_b32_e32 v7, 1, v4
	v_and_b32_e32 v8, 0x7fffffe0, v4
	v_sub_u32_e32 v4, v6, v4
	v_and_b32_e32 v7, 30, v7
	v_add_u32_e32 v4, v4, v8
	v_add3_u32 v6, v4, v7, v5
	s_or_b64 exec, exec, s[6:7]
	s_lshl_b32 s4, s9, 1
	v_lshl_add_u64 v[4:5], v[160:161], 0, s[4:5]
	v_mad_i64_i32 v[6:7], s[6:7], v6, s64, v[4:5]
	ds_read2_b32 v[8:9], v190 offset0:8 offset1:41
	ds_read2_b32 v[10:11], v190 offset0:74 offset1:107
	ds_read2_b32 v[12:13], v190 offset0:140 offset1:173
	ds_read2_b32 v[14:15], v190 offset0:206 offset1:239
	global_store_dwordx4 v[6:7], v[0:3], off nt
	v_add_u32_e32 v6, s8, v191
	v_mul_hi_i32 v7, v6, s62
	s_waitcnt lgkmcnt(3)
	v_cvt_pk_bf16_f32 v0, v8, v9
	v_lshrrev_b32_e32 v8, 31, v7
	v_lshrrev_b32_e32 v7, 5, v7
	v_add_u32_e32 v7, v7, v8
	v_mul_lo_u32 v7, v7, s58
	v_sub_u32_e32 v7, v6, v7
	v_cmp_lt_i32_e32 vcc, s63, v7
	s_waitcnt lgkmcnt(2)
	v_cvt_pk_bf16_f32 v1, v10, v11
	s_waitcnt lgkmcnt(1)
	v_cvt_pk_bf16_f32 v2, v12, v13
	s_waitcnt lgkmcnt(0)
	v_cvt_pk_bf16_f32 v3, v14, v15
	s_and_saveexec_b64 s[6:7], vcc
	v_lshlrev_b32_e32 v9, 1, v7
	v_and_b32_e32 v10, 0x7fffffe0, v7
	v_sub_u32_e32 v6, v6, v7
	v_bfe_u32 v8, v7, 4, 1
	v_and_b32_e32 v9, 30, v9
	v_add_u32_e32 v6, v6, v10
	v_add3_u32 v6, v6, v9, v8
	s_or_b64 exec, exec, s[6:7]
	v_mad_i64_i32 v[6:7], s[6:7], v6, s64, v[4:5]
	ds_read2_b32 v[8:9], v190 offset0:16 offset1:49
	ds_read2_b32 v[10:11], v190 offset0:82 offset1:115
	ds_read2_b32 v[12:13], v190 offset0:148 offset1:181
	ds_read2_b32 v[14:15], v190 offset0:214 offset1:247
	global_store_dwordx4 v[6:7], v[0:3], off nt
	v_add_u32_e32 v6, s8, v192
	v_mul_hi_i32 v7, v6, s62
	s_waitcnt lgkmcnt(3)
	v_cvt_pk_bf16_f32 v0, v8, v9
	v_lshrrev_b32_e32 v8, 31, v7
	v_lshrrev_b32_e32 v7, 5, v7
	v_add_u32_e32 v7, v7, v8
	v_mul_lo_u32 v7, v7, s58
	v_sub_u32_e32 v7, v6, v7
	v_cmp_lt_i32_e32 vcc, s63, v7
	s_waitcnt lgkmcnt(2)
	v_cvt_pk_bf16_f32 v1, v10, v11
	s_waitcnt lgkmcnt(1)
	v_cvt_pk_bf16_f32 v2, v12, v13
	s_waitcnt lgkmcnt(0)
	v_cvt_pk_bf16_f32 v3, v14, v15
	s_and_saveexec_b64 s[6:7], vcc
	v_lshlrev_b32_e32 v9, 1, v7
	v_and_b32_e32 v10, 0x7fffffe0, v7
	v_sub_u32_e32 v6, v6, v7
	v_bfe_u32 v8, v7, 4, 1
	v_and_b32_e32 v9, 30, v9
	v_add_u32_e32 v6, v6, v10
	v_add3_u32 v6, v6, v9, v8
	s_or_b64 exec, exec, s[6:7]
	v_mad_i64_i32 v[6:7], s[6:7], v6, s64, v[4:5]
	ds_read2_b32 v[8:9], v190 offset0:24 offset1:57
	ds_read2_b32 v[10:11], v190 offset0:90 offset1:123
	ds_read2_b32 v[12:13], v190 offset0:156 offset1:189
	ds_read2_b32 v[14:15], v190 offset0:222 offset1:255
	global_store_dwordx4 v[6:7], v[0:3], off nt
	v_add_u32_e32 v6, s8, v193
	v_mul_hi_i32 v7, v6, s62
	s_waitcnt lgkmcnt(3)
	v_cvt_pk_bf16_f32 v0, v8, v9
	v_lshrrev_b32_e32 v8, 31, v7
	v_lshrrev_b32_e32 v7, 5, v7
	v_add_u32_e32 v7, v7, v8
	v_mul_lo_u32 v7, v7, s58
	v_sub_u32_e32 v7, v6, v7
	v_cmp_lt_i32_e32 vcc, s63, v7
	s_waitcnt lgkmcnt(2)
	v_cvt_pk_bf16_f32 v1, v10, v11
	s_waitcnt lgkmcnt(1)
	v_cvt_pk_bf16_f32 v2, v12, v13
	s_waitcnt lgkmcnt(0)
	v_cvt_pk_bf16_f32 v3, v14, v15
	s_and_saveexec_b64 s[6:7], vcc
	v_lshlrev_b32_e32 v9, 1, v7
	v_and_b32_e32 v10, 0x7fffffe0, v7
	v_sub_u32_e32 v6, v6, v7
	v_bfe_u32 v8, v7, 4, 1
	v_and_b32_e32 v9, 30, v9
	v_add_u32_e32 v6, v6, v10
	v_add3_u32 v6, v6, v9, v8
	s_or_b64 exec, exec, s[6:7]
	v_mad_i64_i32 v[4:5], s[6:7], v6, s64, v[4:5]
	global_store_dwordx4 v[4:5], v[0:3], off nt
	s_waitcnt lgkmcnt(0)

; #define LAS __attribute__((address_space(3)))
; __device__ __forceinline__ void transpose_item_fp8(const float* W, int K, int N, unsigned char* WT, float q, LAS float* scr, int item, int lane) {
;     const int nblk = N / 32, kb = item / nblk, nb = item % nblk, k0 = 64 * kb, n0 = 32 * nb;
; #pragma unroll 8
;     for (int i = 0; i < 32; ++i) { const int kk = 2 * i + (lane >> 5); scr[kk * 33 + (lane & 31)] = W[(size_t)(k0 + kk) * N + n0 + (lane & 31)]; }
;     asm volatile("s_waitcnt lgkmcnt(0)" ::: "memory");
.LBB0_72:
	s_lshl_b32 s67, s7, 1
	s_lshl_b32 s70, s4, 1
	v_add_u32_e32 v18, s67, v2
	v_add_u32_e32 v20, s70, v3
	v_add_u32_e32 v22, s67, v4
	v_add_u32_e32 v24, s70, v5
	v_add_u32_e32 v26, s67, v6
	v_add_u32_e32 v28, s70, v7
	v_add_u32_e32 v30, s67, v8
	v_add_u32_e32 v32, s70, v9
	v_add_u32_e32 v34, s67, v10
	v_add_u32_e32 v36, s70, v11
	v_add_u32_e32 v38, s67, v12
	v_add_u32_e32 v40, s70, v13
	v_add_u32_e32 v42, s67, v14
	v_add_u32_e32 v44, s70, v15
	v_add_u32_e32 v46, s67, v16
	v_add_u32_e32 v48, s70, v17
	v_mad_i64_i32 v[18:19], s[68:69], v18, s65, v[0:1]
	v_mad_i64_i32 v[20:21], s[68:69], v20, s65, v[0:1]
	v_mad_i64_i32 v[22:23], s[68:69], v22, s65, v[0:1]
	v_mad_i64_i32 v[24:25], s[68:69], v24, s65, v[0:1]
	v_mad_i64_i32 v[26:27], s[68:69], v26, s65, v[0:1]
	v_mad_i64_i32 v[28:29], s[68:69], v28, s65, v[0:1]
	v_mad_i64_i32 v[30:31], s[68:69], v30, s65, v[0:1]
	v_mad_i64_i32 v[32:33], s[68:69], v32, s65, v[0:1]
	v_mad_i64_i32 v[34:35], s[68:69], v34, s65, v[0:1]
	v_mad_i64_i32 v[36:37], s[68:69], v36, s65, v[0:1]
	v_mad_i64_i32 v[38:39], s[68:69], v38, s65, v[0:1]
	v_mad_i64_i32 v[40:41], s[68:69], v40, s65, v[0:1]
	v_mad_i64_i32 v[42:43], s[68:69], v42, s65, v[0:1]
	v_mad_i64_i32 v[44:45], s[68:69], v44, s65, v[0:1]
	v_mad_i64_i32 v[46:47], s[68:69], v46, s65, v[0:1]
	v_mad_i64_i32 v[48:49], s[68:69], v48, s65, v[0:1]
	global_load_dword v50, v[18:19], off nt
	global_load_dword v51, v[20:21], off nt
	global_load_dword v52, v[22:23], off nt
	global_load_dword v53, v[24:25], off nt
	global_load_dword v54, v[26:27], off nt
	global_load_dword v55, v[28:29], off nt
	global_load_dword v56, v[30:31], off nt
	global_load_dword v57, v[32:33], off nt
	global_load_dword v58, v[34:35], off nt
	global_load_dword v59, v[36:37], off nt
	global_load_dword v60, v[38:39], off nt
	global_load_dword v61, v[40:41], off nt
	global_load_dword v62, v[42:43], off nt
	global_load_dword v63, v[44:45], off nt
	global_load_dword v64, v[46:47], off nt
	global_load_dword v65, v[48:49], off nt
	s_add_i32 s7, s7, 16
	s_add_i32 s4, s4, 16
	s_add_i32 s9, s9, -16
	v_add_u32_e32 v18, s67, v146
	v_add_u32_e32 v20, s70, v141
	v_add_u32_e32 v22, s67, v166
	v_add_u32_e32 v24, s70, v147
	v_add_u32_e32 v26, s67, v168
	v_add_u32_e32 v28, s70, v151
	v_add_u32_e32 v30, s67, v170
	v_add_u32_e32 v32, s70, v167
	v_add_u32_e32 v34, s67, v172
	v_add_u32_e32 v36, s70, v169
	v_add_u32_e32 v38, s67, v174
	v_add_u32_e32 v40, s70, v171
	v_add_u32_e32 v42, s67, v176
	v_add_u32_e32 v44, s70, v173
	v_add_u32_e32 v46, s67, v178
	v_add_u32_e32 v48, s70, v175
	s_cmp_lg_u32 s9, 0
	v_mad_u64_u32 v[18:19], s[68:69], v18, s13, v[150:151]
	v_mad_u64_u32 v[20:21], s[68:69], v20, s13, v[150:151]
	v_mad_u64_u32 v[22:23], s[68:69], v22, s13, v[150:151]
	v_mad_u64_u32 v[24:25], s[68:69], v24, s13, v[150:151]
	v_mad_u64_u32 v[26:27], s[68:69], v26, s13, v[150:151]
	v_mad_u64_u32 v[28:29], s[68:69], v28, s13, v[150:151]
	v_mad_u64_u32 v[30:31], s[68:69], v30, s13, v[150:151]
	v_mad_u64_u32 v[32:33], s[68:69], v32, s13, v[150:151]
	v_mad_u64_u32 v[34:35], s[68:69], v34, s13, v[150:151]
	v_mad_u64_u32 v[36:37], s[68:69], v36, s13, v[150:151]
	v_mad_u64_u32 v[38:39], s[68:69], v38, s13, v[150:151]
	v_mad_u64_u32 v[40:41], s[68:69], v40, s13, v[150:151]
	v_mad_u64_u32 v[42:43], s[68:69], v42, s13, v[150:151]
	v_mad_u64_u32 v[44:45], s[68:69], v44, s13, v[150:151]
	v_mad_u64_u32 v[46:47], s[68:69], v46, s13, v[150:151]
	v_mad_u64_u32 v[48:49], s[68:69], v48, s13, v[150:151]
	s_waitcnt vmcnt(15)
	ds_write_b32 v18, v50
	s_waitcnt vmcnt(14)
	ds_write_b32 v20, v51
	s_waitcnt vmcnt(13)
	ds_write_b32 v22, v52
	s_waitcnt vmcnt(12)
	ds_write_b32 v24, v53
	s_waitcnt vmcnt(11)
	ds_write_b32 v26, v54
	s_waitcnt vmcnt(10)
	ds_write_b32 v28, v55
	s_waitcnt vmcnt(9)
	ds_write_b32 v30, v56
	s_waitcnt vmcnt(8)
	ds_write_b32 v32, v57
	s_waitcnt vmcnt(7)
	ds_write_b32 v34, v58
	s_waitcnt vmcnt(6)
	ds_write_b32 v36, v59
	s_waitcnt vmcnt(5)
	ds_write_b32 v38, v60
	s_waitcnt vmcnt(4)
	ds_write_b32 v40, v61
	s_waitcnt vmcnt(3)
	ds_write_b32 v42, v62
	s_waitcnt vmcnt(2)
	ds_write_b32 v44, v63
	s_waitcnt vmcnt(1)
	ds_write_b32 v46, v64
	s_waitcnt vmcnt(0)
	ds_write_b32 v48, v65
	s_cbranch_scc1 .LBB0_72
; #define LAS __attribute__((address_space(3)))
; __device__ __forceinline__ unsigned pk4_fp8(float x0, float x1, float x2, float x3) { int w = 0; w = __builtin_amdgcn_cvt_pk_fp8_f32(x0, x1, w, false); w = __builtin_amdgcn_cvt_pk_fp8_f32(x2, x3, w, true); return (unsigned)w; }
; __device__ __forceinline__ void transpose_item_fp8(const float* W, int K, int N, unsigned char* WT, float q, LAS float* scr, int item, int lane) {
;     ...
;     const int c = lane & 7;
; #pragma unroll
;     for (int j = 0; j < 4; ++j) { const int n = (lane >> 3) + 8 * j; const LAS float* s = scr + (8 * c) * 33 + n;
;         u32x2 o; o.x = pk4_fp8(s[0 * 33] * q, s[1 * 33] * q, s[2 * 33] * q, s[3 * 33] * q); o.y = pk4_fp8(s[4 * 33] * q, s[5 * 33] * q, s[6 * 33] * q, s[7 * 33] * q);
;         *(u32x2*)(WT + (size_t)(n0 + n) * K + k0 + 8 * c) = o; }
;     asm volatile("s_waitcnt lgkmcnt(0)" ::: "memory");
; }
	s_waitcnt lgkmcnt(0)
	ds_read2_b32 v[0:1], v190 offset1:8
	ds_read2_b32 v[2:3], v190 offset0:33 offset1:41
	ds_read2_b32 v[4:5], v190 offset0:66 offset1:74
	ds_read2_b32 v[8:9], v190 offset0:99 offset1:107
	ds_read2_b32 v[10:11], v190 offset0:132 offset1:140
	ds_read2_b32 v[12:13], v190 offset0:165 offset1:173
	v_mov_b32_e32 v14, 0
	s_waitcnt lgkmcnt(5)
	v_mul_f32_e32 v0, 0x43000000, v0
	s_waitcnt lgkmcnt(4)
	v_mul_f32_e32 v2, 0x43000000, v2
	ds_read2_b32 v[16:17], v190 offset0:198 offset1:206
	ds_read2_b32 v[18:19], v190 offset0:231 offset1:239
	v_cvt_pk_fp8_f32 v14, v0, v2
	s_waitcnt lgkmcnt(3)
	v_mul_f32_e32 v0, 0x43000000, v10
	s_waitcnt lgkmcnt(2)
	v_mul_f32_e32 v2, 0x43000000, v12
	v_mov_b32_e32 v15, 0
	v_cvt_pk_fp8_f32 v15, v0, v2
	s_waitcnt lgkmcnt(1)
	v_mul_f32_e32 v0, 0x43000000, v16
	s_waitcnt lgkmcnt(0)
	v_mul_f32_e32 v2, 0x43000000, v18
	v_mul_f32_e32 v1, 0x43000000, v1
	v_cvt_pk_fp8_f32 v15, v0, v2 op_sel:[0,0,1]
	v_mul_f32_e32 v2, 0x43000000, v3
	v_mov_b32_e32 v0, 0
	v_mul_f32_e32 v3, 0x43000000, v5
	v_cvt_pk_fp8_f32 v0, v1, v2
	v_mul_f32_e32 v2, 0x43000000, v11
	v_mul_f32_e32 v5, 0x43000000, v13
	v_mov_b32_e32 v1, 0
	v_cvt_pk_fp8_f32 v1, v2, v5
	v_mul_f32_e32 v4, 0x43000000, v4
	v_mul_f32_e32 v8, 0x43000000, v8
	v_cvt_pk_fp8_f32 v14, v4, v8 op_sel:[0,0,1]
	v_mul_f32_e32 v4, 0x43000000, v9
	v_add_u32_e32 v20, s6, v189
	v_cvt_pk_fp8_f32 v0, v3, v4 op_sel:[0,0,1]
	v_mul_f32_e32 v2, 0x43000000, v17
	v_mul_f32_e32 v3, 0x43000000, v19
	s_ashr_i32 s9, s8, 31
	v_ashrrev_i32_e32 v21, 31, v20
	v_cvt_pk_fp8_f32 v1, v2, v3 op_sel:[0,0,1]
	v_add_u32_e32 v2, s6, v191
	v_lshl_add_u64 v[6:7], v[164:165], 0, s[8:9]
	v_lshlrev_b64 v[20:21], 10, v[20:21]
	v_ashrrev_i32_e32 v3, 31, v2
	v_lshl_add_u64 v[20:21], v[6:7], 0, v[20:21]
	v_lshlrev_b64 v[2:3], 10, v[2:3]
	global_store_dwordx2 v[20:21], v[14:15], off nt
	v_lshl_add_u64 v[2:3], v[6:7], 0, v[2:3]
	ds_read2_b32 v[4:5], v190 offset0:16 offset1:24
	ds_read2_b32 v[8:9], v190 offset0:49 offset1:57
	ds_read2_b32 v[10:11], v190 offset0:82 offset1:90
	global_store_dwordx2 v[2:3], v[0:1], off nt
	ds_read2_b32 v[0:1], v190 offset0:115 offset1:123
	ds_read2_b32 v[2:3], v190 offset0:148 offset1:156
	ds_read2_b32 v[12:13], v190 offset0:181 offset1:189
	s_waitcnt lgkmcnt(5)
	v_mul_f32_e32 v4, 0x43000000, v4
	s_waitcnt lgkmcnt(4)
	v_mul_f32_e32 v8, 0x43000000, v8
	v_mov_b32_e32 v14, 0
	ds_read2_b32 v[16:17], v190 offset0:214 offset1:222
	ds_read2_b32 v[18:19], v190 offset0:247 offset1:255
	v_cvt_pk_fp8_f32 v14, v4, v8
	s_waitcnt lgkmcnt(3)
	v_mul_f32_e32 v2, 0x43000000, v2
	s_waitcnt lgkmcnt(2)
	v_mul_f32_e32 v4, 0x43000000, v12
	v_mov_b32_e32 v15, 0
	v_cvt_pk_fp8_f32 v15, v2, v4
	v_mul_f32_e32 v10, 0x43000000, v10
	v_mul_f32_e32 v0, 0x43000000, v0
	v_cvt_pk_fp8_f32 v14, v10, v0 op_sel:[0,0,1]
	s_waitcnt lgkmcnt(1)
	v_mul_f32_e32 v0, 0x43000000, v16
	s_waitcnt lgkmcnt(0)
	v_mul_f32_e32 v2, 0x43000000, v18
	v_cvt_pk_fp8_f32 v15, v0, v2 op_sel:[0,0,1]
	v_mul_f32_e32 v2, 0x43000000, v5
	v_mul_f32_e32 v4, 0x43000000, v9
	v_mov_b32_e32 v0, 0
	v_mul_f32_e32 v8, 0x43000000, v1
	v_cvt_pk_fp8_f32 v0, v2, v4
	v_mul_f32_e32 v2, 0x43000000, v3
	v_mul_f32_e32 v3, 0x43000000, v13
	v_mov_b32_e32 v1, 0
	v_cvt_pk_fp8_f32 v1, v2, v3
	v_mul_f32_e32 v5, 0x43000000, v11
	v_mul_f32_e32 v2, 0x43000000, v17
	v_mul_f32_e32 v3, 0x43000000, v19
	v_add_u32_e32 v20, s6, v192
	v_cvt_pk_fp8_f32 v0, v5, v8 op_sel:[0,0,1]
	v_cvt_pk_fp8_f32 v1, v2, v3 op_sel:[0,0,1]
	v_add_u32_e32 v2, s6, v193
	v_ashrrev_i32_e32 v21, 31, v20
	v_ashrrev_i32_e32 v3, 31, v2
	v_lshlrev_b64 v[20:21], 10, v[20:21]
	v_lshlrev_b64 v[2:3], 10, v[2:3]
	v_lshl_add_u64 v[20:21], v[6:7], 0, v[20:21]
	v_lshl_add_u64 v[2:3], v[6:7], 0, v[2:3]
	global_store_dwordx2 v[20:21], v[14:15], off nt
	global_store_dwordx2 v[2:3], v[0:1], off nt
	s_waitcnt lgkmcnt(0)
	s_branch .LBB0_37
